# v14 + diff DMAs in SGPR-base form + de-burst LDS-DMA issue: waves 4-7 issue K/V pieces after first four QK MFMAs (diff copies 2-4, MLA main loop 4 copies)
# speedup vs baseline: 1.0181x; 1.0106x over previous
; #define LAS __attribute__((address_space(3)))
; __device__ __forceinline__ int v_rd_base(int lane) { return ((lane & 3) << 3) | (((lane >> 2) & 3) << 6) | (((lane >> 4) & 1) << 5) | (((lane >> 5) & 1) << 8); }
; #define DMA_WAIT(last) do { if (last) asm volatile("s_waitcnt vmcnt(0)" ::: "memory"); else asm volatile("s_waitcnt vmcnt(%0)" :: "n"(NPW) : "memory"); } while (0)
; template <int DK, int DV, bool OFF, class QLoader> ...
;     ...
;   unsigned koff[KPW], voff[VPW];
; #pragma unroll
;   for (int i = 0; i < (DK == 64 ? 1 : KPW); ++i) { const int row = (wid * KPW + i) * 4 + (lane >> 4); int c = (lane & 15) ^ (row & 7); c = (c < DK / 8) ? c : (c & 7); koff[i] = (unsigned)((row * ldk) * 2 + c * 16); }
; #pragma unroll
;   for (int i = 0; i < 1; ++i) { const int sidx = (wid * VPW + i) * 2 + (lane >> 5), kg = sidx / ND, st = sidx % ND, kk = kg * 8 + ((lane & 31) >> 2);
;     const int k = (kk & ~0xC) | ((kk & 4) << 1) | ((kk & 8) >> 1), c = st * 32 + (lane & 3) * 8; voff[i] = (unsigned)((k * ldv + c) * 2); }
;   const int vb0 = (int)(uintptr_t)V_lds + v_rd_base(lane);
;   LAS unsigned* const ldsK = (LAS unsigned*)(LAS char*)K_lds + (wid * KPW) * 256; LAS unsigned* const ldsV = (LAS unsigned*)(LAS char*)V_lds + (wid * VPW) * 256;
;     ...
;   f32x16 pA0, pA1, pB0, pB1; bf16x8 pa0, pa1, pa2, pa3; const int NT = nkeys / KVBLK;
;   DMA_TILE(0, 0); DMA_TILE(1, 1); DMA_WAIT(false); __syncthreads(); if (2 < NT) DMA_TILE(2, 2);
;   qkt<DK>(pA0, pA1, K_lds, qr, r32, hi); partialSM<DK, OFF>(pA0, pA1, negMC);
;     ...
;   if (wid >= 4) __builtin_amdgcn_s_setprio(1);
;   for (int j = 1; j < NT; j += 4) {
.LBB0_841:
	s_add_u32 s93, s16, 0x8000
	v_and_b32_e32 v25, 63, v25
	s_addc_u32 s94, s17, 0
	s_nop 4
	v_exp_f32_e32 v174, v3
	s_and_b64 s[24:25], s[14:15], exec
	v_lshlrev_b32_e32 v3, 4, v25
	v_exp_f32_e32 v173, v2
	v_exp_f32_e32 v175, v4
	s_cselect_b32 s95, 0x44, 4
	v_lshlrev_b32_e32 v2, 3, v25
	v_and_b32_e32 v3, 0xc0, v3
	v_lshlrev_b32_e32 v4, 1, v25
	s_cmp_lg_u32 0, -1
	v_and_or_b32 v3, v2, 24, v3
	v_and_b32_e32 v4, 32, v4
	v_and_b32_e32 v2, 0x100, v2
	s_cselect_b32 s24, 0, 0
	v_or3_b32 v2, v3, v4, v2
	s_add_i32 s25, s24, 0x4000
	v_add_u32_e32 v169, s24, v2
	v_add_u32_e32 v170, s25, v2
	s_add_i32 s25, s24, 0x8000
	s_add_i32 s24, s24, 0xc000
	v_add_u32_e32 v160, s24, v2
	s_and_b32 s24, s76, 14
	v_add_u32_e32 v171, s25, v2
	s_lshl_b32 s26, s24, 7
	v_add3_u32 v2, v22, v23, v26
	s_movk_i32 s24, 0xc00
	s_add_i32 s96, s95, -1
	s_add_i32 s97, s95, -3
	s_add_i32 s59, s95, -4
	v_mul_lo_u32 v2, v2, s24
	s_add_u32 s2, s2, s26
	v_lshl_add_u32 v2, v20, 5, v2
	v_readlane_b32 s28, v251, 4
	s_addc_u32 s4, s4, 0
	v_or_b32_e32 v2, v2, v24
	v_lshlrev_b32_e32 v3, 7, v21
	v_readlane_b32 s30, v251, 6
	v_sub_u32_e32 v2, v2, v3
	v_readlane_b32 s31, v251, 7
	s_add_u32 s24, s30, s2
	v_lshlrev_b32_e32 v2, 1, v2
	v_mov_b32_e32 v3, v1
	s_addc_u32 s25, s31, s4
	v_mov_b32_e32 v232, v2
	v_lshl_add_u64 v[152:153], s[24:25], 0, v[2:3]
	s_add_u32 s98, s24, s8
	s_addc_u32 s99, s25, s9
	s_add_u32 s24, s30, s78
	s_addc_u32 s25, s31, s77
	v_readlane_b32 s2, v253, 21
	s_add_u32 s60, s2, s78
	v_readlane_b32 s2, v253, 22
	s_addc_u32 s45, s2, s77
	v_exp_f32_e32 v184, v5
	v_exp_f32_e32 v185, v6
	v_exp_f32_e32 v186, v7
	v_exp_f32_e32 v187, v8
	v_exp_f32_e32 v188, v9
	v_exp_f32_e32 v189, v10
	v_exp_f32_e32 v190, v11
	v_exp_f32_e32 v191, v12
	v_exp_f32_e32 v192, v13
	v_exp_f32_e32 v193, v14
	v_exp_f32_e32 v194, v15
	v_exp_f32_e32 v195, v16
	v_exp_f32_e32 v196, v17
	s_add_u32 s2, s80, s26
	v_mov_b32_e32 v2, v0
	s_addc_u32 s5, s79, 0
	v_readlane_b32 s4, v253, 23
	v_mov_b32_e32 v16, v1
	v_mov_b32_e32 v17, v1
	v_lshl_add_u64 v[156:157], s[24:25], 0, v[2:3]
	s_add_u32 s76, s24, s8
	s_addc_u32 s77, s25, s9
	s_mov_b64 s[78:79], s[98:99]
	v_readlane_b32 s80, v251, 12
	s_lshr_b32 s80, s80, 8
	s_add_u32 s4, s4, s2
	v_readlane_b32 s2, v253, 24
	v_mov_b32_e32 v2, v1
	v_mov_b32_e32 v4, v1
	v_mov_b32_e32 v5, v1
	v_mov_b32_e32 v6, v1
	v_mov_b32_e32 v7, v1
	v_mov_b32_e32 v8, v1
	v_mov_b32_e32 v9, v1
	v_mov_b32_e32 v10, v1
	v_mov_b32_e32 v11, v1
	v_mov_b32_e32 v12, v1
	v_mov_b32_e32 v13, v1
	v_mov_b32_e32 v14, v1
	v_mov_b32_e32 v15, v1
	v_mov_b64_e32 v[64:65], v[16:17]
	v_mov_b64_e32 v[48:49], v[16:17]
	v_mov_b64_e32 v[32:33], v[16:17]
	v_lshl_add_u64 v[154:155], s[24:25], 0, v[150:151]
	s_addc_u32 s5, s2, s5
	v_mov_b32_e32 v172, 0
	s_mov_b32 s55, 6
	s_movk_i32 s2, 0xffc0
	v_mov_b64_e32 v[62:63], v[14:15]
	v_mov_b64_e32 v[60:61], v[12:13]
	v_mov_b64_e32 v[58:59], v[10:11]
	v_mov_b64_e32 v[56:57], v[8:9]
	v_mov_b64_e32 v[54:55], v[6:7]
	v_mov_b64_e32 v[52:53], v[4:5]
	v_mov_b64_e32 v[50:51], v[2:3]
	v_mov_b64_e32 v[46:47], v[14:15]
	v_mov_b64_e32 v[44:45], v[12:13]
	v_mov_b64_e32 v[42:43], v[10:11]
	v_mov_b64_e32 v[40:41], v[8:9]
	v_mov_b64_e32 v[38:39], v[6:7]
	v_mov_b64_e32 v[36:37], v[4:5]
	v_mov_b64_e32 v[34:35], v[2:3]
	v_mov_b64_e32 v[30:31], v[14:15]
	v_mov_b64_e32 v[28:29], v[12:13]
	v_mov_b64_e32 v[26:27], v[10:11]
	v_mov_b64_e32 v[24:25], v[8:9]
	v_mov_b64_e32 v[22:23], v[6:7]
	v_mov_b64_e32 v[20:21], v[4:5]
	v_mov_b64_e32 v[18:19], v[2:3]
	v_readlane_b32 s29, v251, 5

.LBB0_855:
	s_add_i32 m0, s81, 0xc000
	s_add_u32 s98, s36, s10
	s_addc_u32 s99, s37, s11
	global_load_lds_dwordx4 v0, s[30:31]
	s_add_i32 m0, s82, 0xc000
	s_nop 0
	global_load_lds_dwordx4 v148, s[36:37]
	s_add_i32 m0, s82, 0xc400
	s_nop 0
	global_load_lds_dwordx4 v148, s[98:99]

; #define DMA_WAIT(last) do { if (last) asm volatile("s_waitcnt vmcnt(0)" ::: "memory"); else asm volatile("s_waitcnt vmcnt(%0)" :: "n"(NPW) : "memory"); } while (0)
; template <int DK, int DV, bool OFF, class QLoader> ...
;     ...
;   f32x16 pA0, pA1, pB0, pB1; bf16x8 pa0, pa1, pa2, pa3; const int NT = nkeys / KVBLK;
;   DMA_TILE(0, 0); DMA_TILE(1, 1); DMA_WAIT(false); __syncthreads(); if (2 < NT) DMA_TILE(2, 2);
;   qkt<DK>(pA0, pA1, K_lds, qr, r32, hi); partialSM<DK, OFF>(pA0, pA1, negMC);
.LBB0_859:
.LBB0_861:
	s_add_i32 s26, s55, -2
	s_cmp_ge_u32 s26, s95
	s_waitcnt vmcnt(0)
	s_barrier
	s_cbranch_scc1 .LBB0_863
	s_cmp_lg_u32 s80, 0
	s_cbranch_scc1 .LBB0_863
	s_add_u32 s98, s76, 0x1ec08000
	s_addc_u32 s99, s77, 0
	s_mov_b32 m0, s81
	s_nop 0
	global_load_lds_dwordx4 v0, s[98:99]
	s_add_u32 s98, s78, 0xdc01000
	s_addc_u32 s99, s79, 0
	s_mov_b32 m0, s82
	s_nop 0
	global_load_lds_dwordx4 v232, s[98:99]
	s_add_u32 s98, s98, 0x80
	s_addc_u32 s99, s99, 0
	s_mov_b32 m0, s84
	s_nop 0
	global_load_lds_dwordx4 v232, s[98:99]
.LBB0_863:
	ds_read_b128 v[66:69], v162 offset:32768
	ds_read_b128 v[70:73], v162 offset:36864
	ds_read_b128 v[130:133], v164 offset:32768
	ds_read_b128 v[134:137], v164 offset:36864
	v_exp_f32_e32 v82, v82
	v_add_f32_e32 v180, 0, v197
	v_add_f32_e32 v180, v200, v180
	v_add_f32_e32 v180, v198, v180
	v_add_f32_e32 v180, v202, v180
	v_add_f32_e32 v180, v204, v180
	v_add_f32_e32 v180, v207, v180
	v_add_f32_e32 v180, v205, v180
	v_add_f32_e32 v180, v210, v180
	v_add_f32_e32 v180, v199, v180
	v_add_f32_e32 v180, v203, v180
	v_add_f32_e32 v180, v201, v180
	v_add_f32_e32 v180, v209, v180
	v_add_f32_e32 v180, v206, v180
	v_add_f32_e32 v180, v211, v180
	v_add_f32_e32 v180, v208, v180
	v_add_f32_e32 v180, v212, v180
	s_waitcnt lgkmcnt(0)
	v_mfma_f32_32x32x16_bf16 v[98:113], v[66:69], v[114:117], 0
	v_exp_f32_e32 v83, v83
	v_exp_f32_e32 v84, v84
	v_exp_f32_e32 v85, v85
	v_exp_f32_e32 v86, v86
	v_exp_f32_e32 v87, v87
	v_exp_f32_e32 v88, v88
	v_exp_f32_e32 v89, v89
	v_mfma_f32_32x32x16_bf16 v[66:81], v[70:73], v[114:117], 0
	v_exp_f32_e32 v90, v90
	v_exp_f32_e32 v91, v91
	v_exp_f32_e32 v92, v92
	v_exp_f32_e32 v93, v93
	v_exp_f32_e32 v94, v94
	v_exp_f32_e32 v95, v95
	v_exp_f32_e32 v96, v96
	v_mfma_f32_32x32x16_bf16 v[98:113], v[130:133], v[118:121], v[98:113]
	v_exp_f32_e32 v97, v97
	v_mfma_f32_32x32x16_bf16 v[66:81], v[134:137], v[118:121], v[66:81]
	s_cmp_eq_u32 s80, 0
	s_cbranch_scc1 .Lstag_2
	s_add_i32 s32, s55, -2
	s_cmp_ge_u32 s32, s95
	s_cbranch_scc1 .Lstag_2
	s_add_u32 s98, s76, 0x1ec08000
	s_addc_u32 s99, s77, 0
	s_mov_b32 m0, s81
	s_nop 0
	global_load_lds_dwordx4 v0, s[98:99]
	s_add_u32 s98, s78, 0xdc01000
	s_addc_u32 s99, s79, 0
	s_mov_b32 m0, s82
	s_nop 0
	global_load_lds_dwordx4 v232, s[98:99]
	s_add_u32 s98, s98, 0x80
	s_addc_u32 s99, s99, 0
	s_mov_b32 m0, s84
	s_nop 0
	global_load_lds_dwordx4 v232, s[98:99]
; __device__ __forceinline__ void finishSM(f32x16& p0, f32x16& p1, float& l_reg, bf16x8& pa0, bf16x8& pa1, bf16x8& pa2, bf16x8& pa3) {
; #pragma unroll
;   for (int r = 0; r < 16; ++r) p1[r] = __builtin_amdgcn_exp2f(p1[r]);
;   float ps = 0;
; #pragma unroll
;   for (int r = 0; r < 16; ++r) ps += p0[r];
; #pragma unroll
;   for (int r = 0; r < 16; ++r) ps += p1[r];
;   l_reg += ps;
;     ...
;   ATT_PK4(p0, 0, pa0); ATT_PK4(p0, 8, pa1); ATT_PK4(p1, 0, pa2); ATT_PK4(p1, 8, pa3);
;     ...
; }
; template <int DK>
; __device__ __forceinline__ void qkt(f32x16& p0, f32x16& p1, const char* Ks, const bf16x8* qr, int r32, int hi) {
;   p0 = f32x16{}; p1 = f32x16{};
; #pragma unroll
;   for (int d0 = 0; d0 < DK / 16; ++d0) { const int cb = (d0 * 16 + hi * 8) * 2;
;     const bf16x8 b0 = *reinterpret_cast<const bf16x8*>(Ks + ATT_KSWZ(r32, cb));
;     const bf16x8 b1 = *reinterpret_cast<const bf16x8*>(Ks + ATT_KSWZ(32 + r32, cb));
;     p0 = __builtin_amdgcn_mfma_f32_32x32x16_bf16(b0, qr[d0], p0, 0, 0, 0);
;     p1 = __builtin_amdgcn_mfma_f32_32x32x16_bf16(b1, qr[d0], p1, 0, 0, 0);
;   }
; }
; template <int DV, int GRP> __device__ __forceinline__ void v_group_read(s16x4* vf, int vb) {
;   sfor<0, 8>([&](auto ic) { constexpr int j = decltype(ic)::value; vf[j] = tr_read<v_rd_off<DV>(GRP, j / 2, j % 2)>(vb); });
; }
; __device__ __forceinline__ void pv_group(f32x16& od, const s16x4* vf, bf16x8 pa0, bf16x8 pa1, bf16x8 pa2, bf16x8 pa3) {
;     ...
;   od = __builtin_amdgcn_mfma_f32_32x32x16_bf16(pa0, ATT_PK(vf[0], vf[1]), od, 0, 0, 0);
;   od = __builtin_amdgcn_mfma_f32_32x32x16_bf16(pa1, ATT_PK(vf[2], vf[3]), od, 0, 0, 0);
;   od = __builtin_amdgcn_mfma_f32_32x32x16_bf16(pa2, ATT_PK(vf[4], vf[5]), od, 0, 0, 0);
;   od = __builtin_amdgcn_mfma_f32_32x32x16_bf16(pa3, ATT_PK(vf[6], vf[7]), od, 0, 0, 0);
;     ...
; }
; template <int DV> __device__ __forceinline__ void pv_all_pipe(f32x16* o, int vb, bf16x8 pa0, bf16x8 pa1, bf16x8 pa2, bf16x8 pa3) {
;   s16x4 va[8], vc[8];
;   v_group_read<DV, 0>(va, vb); v_group_read<DV, 1>(vc, vb);
;   lgkm_wait8<8>(va); pv_group(o[0], va, pa0, pa1, pa2, pa3);
;   if constexpr (DV == 128) {
;     s16x4 vd[8], ve[8];
;     v_group_read<DV, 2>(vd, vb);
;     lgkm_wait8<8>(vc); pv_group(o[1], vc, pa0, pa1, pa2, pa3);
;     v_group_read<DV, 3>(ve, vb);
;     lgkm_wait8<8>(vd); pv_group(o[2], vd, pa0, pa1, pa2, pa3);
;     lgkm_wait8<0>(ve); pv_group(o[3], ve, pa0, pa1, pa2, pa3);
.Lstag_2:
	ds_read_b128 v[130:133], v166 offset:32768
	ds_read_b128 v[134:137], v166 offset:36864
	v_add_f32_e32 v180, v82, v180
	v_add_f32_e32 v180, v83, v180
	v_add_f32_e32 v180, v84, v180
	v_add_f32_e32 v180, v85, v180
	v_add_f32_e32 v180, v86, v180
	v_add_f32_e32 v180, v87, v180
	v_add_f32_e32 v180, v88, v180
	v_add_f32_e32 v180, v89, v180
	s_waitcnt lgkmcnt(0)
	v_mfma_f32_32x32x16_bf16 v[98:113], v[130:133], v[122:125], v[98:113]
	v_mfma_f32_32x32x16_bf16 v[66:81], v[134:137], v[122:125], v[66:81]
	ds_read_b128 v[130:133], v168 offset:32768
	ds_read_b128 v[134:137], v168 offset:36864
	v_add_f32_e32 v180, v90, v180
	v_add_f32_e32 v180, v91, v180
	v_add_f32_e32 v180, v92, v180
	v_add_f32_e32 v180, v93, v180
	v_add_f32_e32 v180, v94, v180
	v_add_f32_e32 v180, v95, v180
	v_add_f32_e32 v180, v96, v180
	v_add_f32_e32 v180, v97, v180
	s_waitcnt lgkmcnt(0)
	v_mfma_f32_32x32x16_bf16 v[98:113], v[130:133], v[126:129], v[98:113]
	v_mfma_f32_32x32x16_bf16 v[66:81], v[134:137], v[126:129], v[66:81]
	v_add_f32_e32 v172, v172, v180
	v_cvt_pk_bf16_f32 v130, v197, v200
	v_cvt_pk_bf16_f32 v131, v198, v202
	v_cvt_pk_bf16_f32 v132, v204, v207
	v_cvt_pk_bf16_f32 v133, v205, v210
	v_cvt_pk_bf16_f32 v134, v199, v203
	v_cvt_pk_bf16_f32 v135, v201, v209
	v_cvt_pk_bf16_f32 v136, v206, v211
	v_cvt_pk_bf16_f32 v137, v208, v212
	v_cvt_pk_bf16_f32 v138, v82, v83
	v_cvt_pk_bf16_f32 v139, v84, v85
	v_cvt_pk_bf16_f32 v140, v86, v87
	v_cvt_pk_bf16_f32 v141, v88, v89
	v_cvt_pk_bf16_f32 v142, v90, v91
	v_cvt_pk_bf16_f32 v143, v92, v93
	v_cvt_pk_bf16_f32 v144, v94, v95
	v_cvt_pk_bf16_f32 v145, v96, v97
	ds_read_b64_tr_b16 v[174:175], v170 offset:0
	ds_read_b64_tr_b16 v[176:177], v170 offset:0x800
	ds_read_b64_tr_b16 v[184:185], v170 offset:0x1000
	ds_read_b64_tr_b16 v[186:187], v170 offset:0x1800
	ds_read_b64_tr_b16 v[188:189], v170 offset:0x2000
	ds_read_b64_tr_b16 v[190:191], v170 offset:0x2800
	ds_read_b64_tr_b16 v[192:193], v170 offset:0x3000
	ds_read_b64_tr_b16 v[194:195], v170 offset:0x3800
	ds_read_b64_tr_b16 v[214:215], v170 offset:0x200
	ds_read_b64_tr_b16 v[216:217], v170 offset:0xa00
	ds_read_b64_tr_b16 v[218:219], v170 offset:0x1200
	s_nop 0
	v_permlane32_swap_b32_e32 v130, v132
	v_permlane32_swap_b32_e32 v131, v133
	ds_read_b64_tr_b16 v[220:221], v170 offset:0x1a00
	ds_read_b64_tr_b16 v[222:223], v170 offset:0x2200
	ds_read_b64_tr_b16 v[224:225], v170 offset:0x2a00
	ds_read_b64_tr_b16 v[226:227], v170 offset:0x3200
	ds_read_b64_tr_b16 v[228:229], v170 offset:0x3a00
	s_waitcnt lgkmcnt(8)
	v_permlane32_swap_b32_e32 v134, v136
	s_nop 0
	v_mfma_f32_32x32x16_bf16 v[2:17], v[130:133], v[174:177], v[2:17]
	v_permlane32_swap_b32_e32 v135, v137
	v_permlane32_swap_b32_e32 v138, v140
	v_permlane32_swap_b32_e32 v139, v141
	ds_read_b64_tr_b16 v[174:175], v170 offset:0x400
	v_mfma_f32_32x32x16_bf16 v[2:17], v[134:137], v[184:187], v[2:17]
	v_permlane32_swap_b32_e32 v142, v144
	v_permlane32_swap_b32_e32 v143, v145
	ds_read_b64_tr_b16 v[176:177], v170 offset:0xc00
	ds_read_b64_tr_b16 v[184:185], v170 offset:0x1400
	ds_read_b64_tr_b16 v[186:187], v170 offset:0x1c00
	v_mfma_f32_32x32x16_bf16 v[2:17], v[138:141], v[188:191], v[2:17]
	ds_read_b64_tr_b16 v[188:189], v170 offset:0x2400
	ds_read_b64_tr_b16 v[190:191], v170 offset:0x2c00
	v_exp_f32_e32 v173, v98
	v_exp_f32_e32 v196, v113
	v_mfma_f32_32x32x16_bf16 v[2:17], v[142:145], v[192:195], v[2:17]
	ds_read_b64_tr_b16 v[192:193], v170 offset:0x3400
	ds_read_b64_tr_b16 v[194:195], v170 offset:0x3c00
	s_waitcnt lgkmcnt(8)
	s_nop 0
	v_mfma_f32_32x32x16_bf16 v[50:65], v[130:133], v[214:217], v[50:65]
	ds_read_b64_tr_b16 v[214:215], v170 offset:0x600
	ds_read_b64_tr_b16 v[216:217], v170 offset:0xe00
	v_mfma_f32_32x32x16_bf16 v[50:65], v[134:137], v[218:221], v[50:65]
	ds_read_b64_tr_b16 v[218:219], v170 offset:0x1600
	ds_read_b64_tr_b16 v[220:221], v170 offset:0x1e00
	v_mfma_f32_32x32x16_bf16 v[50:65], v[138:141], v[222:225], v[50:65]
	ds_read_b64_tr_b16 v[222:223], v170 offset:0x2600
	ds_read_b64_tr_b16 v[224:225], v170 offset:0x2e00
	v_mfma_f32_32x32x16_bf16 v[50:65], v[142:145], v[226:229], v[50:65]
	ds_read_b64_tr_b16 v[226:227], v170 offset:0x3600
	ds_read_b64_tr_b16 v[228:229], v170 offset:0x3e00
	s_waitcnt lgkmcnt(8)
	s_nop 0
	s_waitcnt lgkmcnt(0)
	v_mfma_f32_32x32x16_bf16 v[34:49], v[130:133], v[174:177], v[34:49]
	v_exp_f32_e32 v174, v99
	v_exp_f32_e32 v175, v100
	v_mfma_f32_32x32x16_bf16 v[18:33], v[130:133], v[214:217], v[18:33]
	v_mfma_f32_32x32x16_bf16 v[34:49], v[134:137], v[184:187], v[34:49]
	v_exp_f32_e32 v184, v101
	v_exp_f32_e32 v185, v102
	v_exp_f32_e32 v186, v103
	v_exp_f32_e32 v187, v104
	v_mfma_f32_32x32x16_bf16 v[18:33], v[134:137], v[218:221], v[18:33]
	v_mfma_f32_32x32x16_bf16 v[34:49], v[138:141], v[188:191], v[34:49]
	v_exp_f32_e32 v188, v105
	v_exp_f32_e32 v189, v106
	v_exp_f32_e32 v190, v107
	v_exp_f32_e32 v191, v108
	v_mfma_f32_32x32x16_bf16 v[18:33], v[138:141], v[222:225], v[18:33]
	v_mfma_f32_32x32x16_bf16 v[34:49], v[142:145], v[192:195], v[34:49]
	v_exp_f32_e32 v192, v109
	v_exp_f32_e32 v193, v110
	v_exp_f32_e32 v194, v111
	v_exp_f32_e32 v195, v112
	v_mfma_f32_32x32x16_bf16 v[18:33], v[142:145], v[226:229], v[18:33]
	s_andn2_b64 vcc, exec, s[24:25]
	s_cbranch_vccz .LBB0_866

; #define DMA_WAIT(last) do { if (last) asm volatile("s_waitcnt vmcnt(0)" ::: "memory"); else asm volatile("s_waitcnt vmcnt(%0)" :: "n"(NPW) : "memory"); } while (0)
; template <int DK, int DV, bool OFF, class QLoader> ...
;     ...
;   f32x16 pA0, pA1, pB0, pB1; bf16x8 pa0, pa1, pa2, pa3; const int NT = nkeys / KVBLK;
;   DMA_TILE(0, 0); DMA_TILE(1, 1); DMA_WAIT(false); __syncthreads(); if (2 < NT) DMA_TILE(2, 2);
;   qkt<DK>(pA0, pA1, K_lds, qr, r32, hi); partialSM<DK, OFF>(pA0, pA1, negMC);
.LBB0_868:
.LBB0_870:
	s_add_i32 s24, s55, -1
	s_cmp_ge_u32 s24, s95
	s_waitcnt vmcnt(0)
	s_barrier
	s_cbranch_scc1 .LBB0_872
	s_cmp_lg_u32 s80, 0
	s_cbranch_scc1 .LBB0_872
	s_add_u32 s98, s76, 0x1ec0a000
	s_addc_u32 s99, s77, 0
	s_mov_b32 m0, s85
	s_nop 0
	global_load_lds_dwordx4 v0, s[98:99]
	s_add_u32 s98, s78, 0xdc61000
	s_addc_u32 s99, s79, 0
	s_mov_b32 m0, s87
	s_nop 0
	global_load_lds_dwordx4 v232, s[98:99]
	s_add_u32 s98, s98, 0x80
	s_addc_u32 s99, s99, 0
	s_mov_b32 m0, s88
	s_nop 0
	global_load_lds_dwordx4 v232, s[98:99]
.LBB0_872:
	ds_read_b128 v[82:85], v162 offset:49152
	ds_read_b128 v[86:89], v162 offset:53248
	ds_read_b128 v[130:133], v164 offset:49152
	ds_read_b128 v[134:137], v164 offset:53248
	v_exp_f32_e32 v66, v66
	v_add_f32_e32 v180, 0, v173
	v_add_f32_e32 v180, v174, v180
	v_add_f32_e32 v180, v175, v180
	v_add_f32_e32 v180, v184, v180
	v_add_f32_e32 v180, v185, v180
	v_add_f32_e32 v180, v186, v180
	v_add_f32_e32 v180, v187, v180
	v_add_f32_e32 v180, v188, v180
	v_add_f32_e32 v180, v189, v180
	v_add_f32_e32 v180, v190, v180
	v_add_f32_e32 v180, v191, v180
	v_add_f32_e32 v180, v192, v180
	v_add_f32_e32 v180, v193, v180
	v_add_f32_e32 v180, v194, v180
	v_add_f32_e32 v180, v195, v180
	v_add_f32_e32 v180, v196, v180
	s_waitcnt lgkmcnt(0)
	v_mfma_f32_32x32x16_bf16 v[98:113], v[82:85], v[114:117], 0
	v_exp_f32_e32 v67, v67
	v_exp_f32_e32 v68, v68
	v_exp_f32_e32 v69, v69
	v_exp_f32_e32 v70, v70
	v_exp_f32_e32 v71, v71
	v_exp_f32_e32 v72, v72
	v_exp_f32_e32 v73, v73
	v_mfma_f32_32x32x16_bf16 v[82:97], v[86:89], v[114:117], 0
	v_exp_f32_e32 v74, v74
	v_exp_f32_e32 v75, v75
	v_exp_f32_e32 v76, v76
	v_exp_f32_e32 v77, v77
	v_exp_f32_e32 v78, v78
	v_exp_f32_e32 v79, v79
	v_exp_f32_e32 v80, v80
	v_mfma_f32_32x32x16_bf16 v[98:113], v[130:133], v[118:121], v[98:113]
	v_exp_f32_e32 v81, v81
	v_mfma_f32_32x32x16_bf16 v[82:97], v[134:137], v[118:121], v[82:97]
	s_cmp_eq_u32 s80, 0
	s_cbranch_scc1 .Lstag_3
	s_add_i32 s32, s55, -1
	s_cmp_ge_u32 s32, s95
	s_cbranch_scc1 .Lstag_3
	s_add_u32 s98, s76, 0x1ec0a000
	s_addc_u32 s99, s77, 0
	s_mov_b32 m0, s85
	s_nop 0
	global_load_lds_dwordx4 v0, s[98:99]
	s_add_u32 s98, s78, 0xdc61000
	s_addc_u32 s99, s79, 0
	s_mov_b32 m0, s87
	s_nop 0
	global_load_lds_dwordx4 v232, s[98:99]
	s_add_u32 s98, s98, 0x80
	s_addc_u32 s99, s99, 0
	s_mov_b32 m0, s88
	s_nop 0
	global_load_lds_dwordx4 v232, s[98:99]
; __device__ __forceinline__ void finishSM(f32x16& p0, f32x16& p1, float& l_reg, bf16x8& pa0, bf16x8& pa1, bf16x8& pa2, bf16x8& pa3) {
; #pragma unroll
;   for (int r = 0; r < 16; ++r) p1[r] = __builtin_amdgcn_exp2f(p1[r]);
;   float ps = 0;
; #pragma unroll
;   for (int r = 0; r < 16; ++r) ps += p0[r];
; #pragma unroll
;   for (int r = 0; r < 16; ++r) ps += p1[r];
;   l_reg += ps;
;     ...
;   ATT_PK4(p0, 0, pa0); ATT_PK4(p0, 8, pa1); ATT_PK4(p1, 0, pa2); ATT_PK4(p1, 8, pa3);
;     ...
; }
; template <int DK>
; __device__ __forceinline__ void qkt(f32x16& p0, f32x16& p1, const char* Ks, const bf16x8* qr, int r32, int hi) {
;   p0 = f32x16{}; p1 = f32x16{};
; #pragma unroll
;   for (int d0 = 0; d0 < DK / 16; ++d0) { const int cb = (d0 * 16 + hi * 8) * 2;
;     const bf16x8 b0 = *reinterpret_cast<const bf16x8*>(Ks + ATT_KSWZ(r32, cb));
;     const bf16x8 b1 = *reinterpret_cast<const bf16x8*>(Ks + ATT_KSWZ(32 + r32, cb));
;     p0 = __builtin_amdgcn_mfma_f32_32x32x16_bf16(b0, qr[d0], p0, 0, 0, 0);
;     p1 = __builtin_amdgcn_mfma_f32_32x32x16_bf16(b1, qr[d0], p1, 0, 0, 0);
;   }
; }
; template <int DV, int GRP> __device__ __forceinline__ void v_group_read(s16x4* vf, int vb) {
;   sfor<0, 8>([&](auto ic) { constexpr int j = decltype(ic)::value; vf[j] = tr_read<v_rd_off<DV>(GRP, j / 2, j % 2)>(vb); });
; }
; __device__ __forceinline__ void pv_group(f32x16& od, const s16x4* vf, bf16x8 pa0, bf16x8 pa1, bf16x8 pa2, bf16x8 pa3) {
;     ...
;   od = __builtin_amdgcn_mfma_f32_32x32x16_bf16(pa0, ATT_PK(vf[0], vf[1]), od, 0, 0, 0);
;   od = __builtin_amdgcn_mfma_f32_32x32x16_bf16(pa1, ATT_PK(vf[2], vf[3]), od, 0, 0, 0);
;   od = __builtin_amdgcn_mfma_f32_32x32x16_bf16(pa2, ATT_PK(vf[4], vf[5]), od, 0, 0, 0);
;   od = __builtin_amdgcn_mfma_f32_32x32x16_bf16(pa3, ATT_PK(vf[6], vf[7]), od, 0, 0, 0);
;     ...
; }
; template <int DV> __device__ __forceinline__ void pv_all_pipe(f32x16* o, int vb, bf16x8 pa0, bf16x8 pa1, bf16x8 pa2, bf16x8 pa3) {
;   s16x4 va[8], vc[8];
;   v_group_read<DV, 0>(va, vb); v_group_read<DV, 1>(vc, vb);
;   lgkm_wait8<8>(va); pv_group(o[0], va, pa0, pa1, pa2, pa3);
;   if constexpr (DV == 128) {
;     s16x4 vd[8], ve[8];
;     v_group_read<DV, 2>(vd, vb);
;     lgkm_wait8<8>(vc); pv_group(o[1], vc, pa0, pa1, pa2, pa3);
;     v_group_read<DV, 3>(ve, vb);
;     lgkm_wait8<8>(vd); pv_group(o[2], vd, pa0, pa1, pa2, pa3);
;     lgkm_wait8<0>(ve); pv_group(o[3], ve, pa0, pa1, pa2, pa3);
.Lstag_3:
	ds_read_b128 v[130:133], v166 offset:49152
	ds_read_b128 v[134:137], v166 offset:53248
	v_add_f32_e32 v180, v66, v180
	v_add_f32_e32 v180, v67, v180
	v_add_f32_e32 v180, v68, v180
	v_add_f32_e32 v180, v69, v180
	v_add_f32_e32 v180, v70, v180
	v_add_f32_e32 v180, v71, v180
	v_add_f32_e32 v180, v72, v180
	v_add_f32_e32 v180, v73, v180
	s_waitcnt lgkmcnt(0)
	v_mfma_f32_32x32x16_bf16 v[98:113], v[130:133], v[122:125], v[98:113]
	v_mfma_f32_32x32x16_bf16 v[82:97], v[134:137], v[122:125], v[82:97]
	ds_read_b128 v[130:133], v168 offset:49152
	ds_read_b128 v[134:137], v168 offset:53248
	v_add_f32_e32 v180, v74, v180
	v_add_f32_e32 v180, v75, v180
	v_add_f32_e32 v180, v76, v180
	v_add_f32_e32 v180, v77, v180
	v_add_f32_e32 v180, v78, v180
	v_add_f32_e32 v180, v79, v180
	v_add_f32_e32 v180, v80, v180
	v_add_f32_e32 v180, v81, v180
	s_waitcnt lgkmcnt(0)
	v_mfma_f32_32x32x16_bf16 v[98:113], v[130:133], v[126:129], v[98:113]
	v_mfma_f32_32x32x16_bf16 v[82:97], v[134:137], v[126:129], v[82:97]
	v_add_f32_e32 v172, v172, v180
	v_cvt_pk_bf16_f32 v130, v173, v174
	v_cvt_pk_bf16_f32 v131, v175, v184
	v_cvt_pk_bf16_f32 v132, v185, v186
	v_cvt_pk_bf16_f32 v133, v187, v188
	v_cvt_pk_bf16_f32 v134, v189, v190
	v_cvt_pk_bf16_f32 v135, v191, v192
	v_cvt_pk_bf16_f32 v136, v193, v194
	v_cvt_pk_bf16_f32 v137, v195, v196
	v_cvt_pk_bf16_f32 v138, v66, v67
	v_cvt_pk_bf16_f32 v139, v68, v69
	v_cvt_pk_bf16_f32 v140, v70, v71
	v_cvt_pk_bf16_f32 v141, v72, v73
	v_cvt_pk_bf16_f32 v142, v74, v75
	v_cvt_pk_bf16_f32 v143, v76, v77
	v_cvt_pk_bf16_f32 v144, v78, v79
	v_cvt_pk_bf16_f32 v145, v80, v81
	ds_read_b64_tr_b16 v[176:177], v171 offset:0
	ds_read_b64_tr_b16 v[178:179], v171 offset:0x800
	ds_read_b64_tr_b16 v[198:199], v171 offset:0x1000
	ds_read_b64_tr_b16 v[200:201], v171 offset:0x1800
	ds_read_b64_tr_b16 v[202:203], v171 offset:0x2000
	ds_read_b64_tr_b16 v[204:205], v171 offset:0x2800
	ds_read_b64_tr_b16 v[206:207], v171 offset:0x3000
	ds_read_b64_tr_b16 v[208:209], v171 offset:0x3800
	ds_read_b64_tr_b16 v[210:211], v171 offset:0x200
	ds_read_b64_tr_b16 v[212:213], v171 offset:0xa00
	ds_read_b64_tr_b16 v[214:215], v171 offset:0x1200
	s_nop 0
	v_permlane32_swap_b32_e32 v130, v132
	v_permlane32_swap_b32_e32 v131, v133
	ds_read_b64_tr_b16 v[216:217], v171 offset:0x1a00
	ds_read_b64_tr_b16 v[218:219], v171 offset:0x2200
	ds_read_b64_tr_b16 v[220:221], v171 offset:0x2a00
	ds_read_b64_tr_b16 v[222:223], v171 offset:0x3200
	ds_read_b64_tr_b16 v[224:225], v171 offset:0x3a00
	s_waitcnt lgkmcnt(8)
	v_permlane32_swap_b32_e32 v134, v136
	s_nop 0
	v_mfma_f32_32x32x16_bf16 v[2:17], v[130:133], v[176:179], v[2:17]
	v_permlane32_swap_b32_e32 v135, v137
	v_permlane32_swap_b32_e32 v138, v140
	v_permlane32_swap_b32_e32 v139, v141
	ds_read_b64_tr_b16 v[176:177], v171 offset:0x400
	v_mfma_f32_32x32x16_bf16 v[2:17], v[134:137], v[198:201], v[2:17]
	v_permlane32_swap_b32_e32 v142, v144
	v_permlane32_swap_b32_e32 v143, v145
	ds_read_b64_tr_b16 v[178:179], v171 offset:0xc00
	ds_read_b64_tr_b16 v[198:199], v171 offset:0x1400
	ds_read_b64_tr_b16 v[200:201], v171 offset:0x1c00
	v_mfma_f32_32x32x16_bf16 v[2:17], v[138:141], v[202:205], v[2:17]
	ds_read_b64_tr_b16 v[202:203], v171 offset:0x2400
	ds_read_b64_tr_b16 v[204:205], v171 offset:0x2c00
	v_exp_f32_e32 v197, v98
	v_mfma_f32_32x32x16_bf16 v[2:17], v[142:145], v[206:209], v[2:17]
	ds_read_b64_tr_b16 v[206:207], v171 offset:0x3400
	ds_read_b64_tr_b16 v[208:209], v171 offset:0x3c00
	s_waitcnt lgkmcnt(8)
	s_nop 0
	v_mfma_f32_32x32x16_bf16 v[50:65], v[130:133], v[210:213], v[50:65]
	ds_read_b64_tr_b16 v[210:211], v171 offset:0x600
	ds_read_b64_tr_b16 v[212:213], v171 offset:0xe00
	v_mfma_f32_32x32x16_bf16 v[50:65], v[134:137], v[214:217], v[50:65]
	ds_read_b64_tr_b16 v[214:215], v171 offset:0x1600
	ds_read_b64_tr_b16 v[216:217], v171 offset:0x1e00
	v_mfma_f32_32x32x16_bf16 v[50:65], v[138:141], v[218:221], v[50:65]
	ds_read_b64_tr_b16 v[218:219], v171 offset:0x2600
	ds_read_b64_tr_b16 v[220:221], v171 offset:0x2e00
	v_mfma_f32_32x32x16_bf16 v[50:65], v[142:145], v[222:225], v[50:65]
	ds_read_b64_tr_b16 v[222:223], v171 offset:0x3600
	ds_read_b64_tr_b16 v[224:225], v171 offset:0x3e00
	s_waitcnt lgkmcnt(8)
	s_nop 0
	s_waitcnt lgkmcnt(0)
	v_mfma_f32_32x32x16_bf16 v[34:49], v[130:133], v[176:179], v[34:49]
	v_mfma_f32_32x32x16_bf16 v[18:33], v[130:133], v[210:213], v[18:33]
	v_exp_f32_e32 v210, v105
	v_exp_f32_e32 v211, v111
	v_exp_f32_e32 v212, v113
	v_mfma_f32_32x32x16_bf16 v[34:49], v[134:137], v[198:201], v[34:49]
	v_exp_f32_e32 v200, v99
	v_exp_f32_e32 v198, v100
	v_exp_f32_e32 v199, v106
	v_exp_f32_e32 v201, v108
	v_mfma_f32_32x32x16_bf16 v[18:33], v[134:137], v[214:217], v[18:33]
	v_mfma_f32_32x32x16_bf16 v[34:49], v[138:141], v[202:205], v[34:49]
	v_exp_f32_e32 v202, v101
	v_exp_f32_e32 v204, v102
	v_exp_f32_e32 v205, v104
	v_exp_f32_e32 v203, v107
	v_mfma_f32_32x32x16_bf16 v[18:33], v[138:141], v[218:221], v[18:33]
	v_mfma_f32_32x32x16_bf16 v[34:49], v[142:145], v[206:209], v[34:49]
	v_exp_f32_e32 v207, v103
	v_exp_f32_e32 v209, v109
	v_exp_f32_e32 v206, v110
	v_exp_f32_e32 v208, v112
	v_mfma_f32_32x32x16_bf16 v[18:33], v[142:145], v[222:225], v[18:33]
	s_cmp_ge_u32 s57, s97
	s_cbranch_scc1 .LBB0_880

; #define DMA_WAIT(last) do { if (last) asm volatile("s_waitcnt vmcnt(0)" ::: "memory"); else asm volatile("s_waitcnt vmcnt(%0)" :: "n"(NPW) : "memory"); } while (0)
; template <int DK, int DV, bool OFF, class QLoader> ...
;     ...
;   f32x16 pA0, pA1, pB0, pB1; bf16x8 pa0, pa1, pa2, pa3; const int NT = nkeys / KVBLK;
;   DMA_TILE(0, 0); DMA_TILE(1, 1); DMA_WAIT(false); __syncthreads(); if (2 < NT) DMA_TILE(2, 2);
;   qkt<DK>(pA0, pA1, K_lds, qr, r32, hi); partialSM<DK, OFF>(pA0, pA1, negMC);
.LBB0_875:
.LBB0_877:
	s_cmp_ge_u32 s55, s95
	s_waitcnt vmcnt(0)
	s_barrier
	s_cbranch_scc1 .LBB0_879
	s_cmp_lg_u32 s80, 0
	s_cbranch_scc1 .LBB0_879
	s_add_u32 s98, s76, 0x1ec0c000
	s_addc_u32 s99, s77, 0
	s_mov_b32 m0, s89
	s_nop 0
	global_load_lds_dwordx4 v0, s[98:99]
	s_add_u32 s98, s78, 0xdcc1000
	s_addc_u32 s99, s79, 0
	s_mov_b32 m0, s91
	s_nop 0
	global_load_lds_dwordx4 v232, s[98:99]
	s_add_u32 s98, s98, 0x80
	s_addc_u32 s99, s99, 0
	s_mov_b32 m0, s92
	s_nop 0
	global_load_lds_dwordx4 v232, s[98:99]
.LBB0_879:
	ds_read_b128 v[66:69], v162
	ds_read_b128 v[70:73], v162 offset:4096
	ds_read_b128 v[130:133], v164
	ds_read_b128 v[134:137], v164 offset:4096
	v_exp_f32_e32 v82, v82
	v_exp_f32_e32 v83, v83
	v_add_f32_e32 v180, 0, v197
	v_add_f32_e32 v180, v200, v180
	v_add_f32_e32 v180, v198, v180
	v_add_f32_e32 v180, v202, v180
	v_add_f32_e32 v180, v204, v180
	v_add_f32_e32 v180, v207, v180
	v_add_f32_e32 v180, v205, v180
	v_add_f32_e32 v180, v210, v180
	v_add_f32_e32 v180, v199, v180
	v_add_f32_e32 v180, v203, v180
	v_add_f32_e32 v180, v201, v180
	v_add_f32_e32 v180, v209, v180
	v_add_f32_e32 v180, v206, v180
	v_add_f32_e32 v180, v211, v180
	v_add_f32_e32 v180, v208, v180
	v_add_f32_e32 v180, v212, v180
	s_waitcnt lgkmcnt(0)
	v_mfma_f32_32x32x16_bf16 v[98:113], v[66:69], v[114:117], 0
	v_exp_f32_e32 v84, v84
	v_exp_f32_e32 v85, v85
	v_exp_f32_e32 v86, v86
	v_exp_f32_e32 v87, v87
	v_exp_f32_e32 v88, v88
	v_exp_f32_e32 v89, v89
	v_exp_f32_e32 v90, v90
	v_mfma_f32_32x32x16_bf16 v[66:81], v[70:73], v[114:117], 0
	v_exp_f32_e32 v91, v91
	v_exp_f32_e32 v92, v92
	v_exp_f32_e32 v93, v93
	v_exp_f32_e32 v94, v94
	v_exp_f32_e32 v95, v95
	v_exp_f32_e32 v96, v96
	v_exp_f32_e32 v97, v97
	v_mfma_f32_32x32x16_bf16 v[98:113], v[130:133], v[118:121], v[98:113]
	v_mfma_f32_32x32x16_bf16 v[66:81], v[134:137], v[118:121], v[66:81]
	s_cmp_eq_u32 s80, 0
	s_cbranch_scc1 .Lstag_4
	s_cmp_ge_u32 s55, s95
	s_cbranch_scc1 .Lstag_4
	s_add_u32 s98, s76, 0x1ec0c000
	s_addc_u32 s99, s77, 0
	s_mov_b32 m0, s89
	s_nop 0
	global_load_lds_dwordx4 v0, s[98:99]
	s_add_u32 s98, s78, 0xdcc1000
	s_addc_u32 s99, s79, 0
	s_mov_b32 m0, s91
	s_nop 0
	global_load_lds_dwordx4 v232, s[98:99]
	s_add_u32 s98, s98, 0x80
	s_addc_u32 s99, s99, 0
	s_mov_b32 m0, s92
	s_nop 0
	global_load_lds_dwordx4 v232, s[98:99]
; __device__ __forceinline__ void finishSM(f32x16& p0, f32x16& p1, float& l_reg, bf16x8& pa0, bf16x8& pa1, bf16x8& pa2, bf16x8& pa3) {
; #pragma unroll
;   for (int r = 0; r < 16; ++r) p1[r] = __builtin_amdgcn_exp2f(p1[r]);
;   float ps = 0;
; #pragma unroll
;   for (int r = 0; r < 16; ++r) ps += p0[r];
; #pragma unroll
;   for (int r = 0; r < 16; ++r) ps += p1[r];
;   l_reg += ps;
;     ...
;   ATT_PK4(p0, 0, pa0); ATT_PK4(p0, 8, pa1); ATT_PK4(p1, 0, pa2); ATT_PK4(p1, 8, pa3);
;     ...
; }
; template <int DK>
; __device__ __forceinline__ void qkt(f32x16& p0, f32x16& p1, const char* Ks, const bf16x8* qr, int r32, int hi) {
;   p0 = f32x16{}; p1 = f32x16{};
; #pragma unroll
;   for (int d0 = 0; d0 < DK / 16; ++d0) { const int cb = (d0 * 16 + hi * 8) * 2;
;     const bf16x8 b0 = *reinterpret_cast<const bf16x8*>(Ks + ATT_KSWZ(r32, cb));
;     const bf16x8 b1 = *reinterpret_cast<const bf16x8*>(Ks + ATT_KSWZ(32 + r32, cb));
;     p0 = __builtin_amdgcn_mfma_f32_32x32x16_bf16(b0, qr[d0], p0, 0, 0, 0);
;     p1 = __builtin_amdgcn_mfma_f32_32x32x16_bf16(b1, qr[d0], p1, 0, 0, 0);
;   }
; }
; template <int DV, int GRP> __device__ __forceinline__ void v_group_read(s16x4* vf, int vb) {
;   sfor<0, 8>([&](auto ic) { constexpr int j = decltype(ic)::value; vf[j] = tr_read<v_rd_off<DV>(GRP, j / 2, j % 2)>(vb); });
; }
; __device__ __forceinline__ void pv_group(f32x16& od, const s16x4* vf, bf16x8 pa0, bf16x8 pa1, bf16x8 pa2, bf16x8 pa3) {
;     ...
;   od = __builtin_amdgcn_mfma_f32_32x32x16_bf16(pa0, ATT_PK(vf[0], vf[1]), od, 0, 0, 0);
;   od = __builtin_amdgcn_mfma_f32_32x32x16_bf16(pa1, ATT_PK(vf[2], vf[3]), od, 0, 0, 0);
;   od = __builtin_amdgcn_mfma_f32_32x32x16_bf16(pa2, ATT_PK(vf[4], vf[5]), od, 0, 0, 0);
;   od = __builtin_amdgcn_mfma_f32_32x32x16_bf16(pa3, ATT_PK(vf[6], vf[7]), od, 0, 0, 0);
;     ...
; }
; template <int DV> __device__ __forceinline__ void pv_all_pipe(f32x16* o, int vb, bf16x8 pa0, bf16x8 pa1, bf16x8 pa2, bf16x8 pa3) {
;   s16x4 va[8], vc[8];
;   v_group_read<DV, 0>(va, vb); v_group_read<DV, 1>(vc, vb);
;   lgkm_wait8<8>(va); pv_group(o[0], va, pa0, pa1, pa2, pa3);
;   if constexpr (DV == 128) {
;     s16x4 vd[8], ve[8];
;     v_group_read<DV, 2>(vd, vb);
;     lgkm_wait8<8>(vc); pv_group(o[1], vc, pa0, pa1, pa2, pa3);
;     v_group_read<DV, 3>(ve, vb);
;     lgkm_wait8<8>(vd); pv_group(o[2], vd, pa0, pa1, pa2, pa3);
;     lgkm_wait8<0>(ve); pv_group(o[3], ve, pa0, pa1, pa2, pa3);
.Lstag_4:
	ds_read_b128 v[130:133], v166
	ds_read_b128 v[134:137], v166 offset:4096
	v_add_f32_e32 v180, v82, v180
	v_add_f32_e32 v180, v83, v180
	v_add_f32_e32 v180, v84, v180
	v_add_f32_e32 v180, v85, v180
	v_add_f32_e32 v180, v86, v180
	v_add_f32_e32 v180, v87, v180
	v_add_f32_e32 v180, v88, v180
	v_add_f32_e32 v180, v89, v180
	s_waitcnt lgkmcnt(0)
	v_mfma_f32_32x32x16_bf16 v[98:113], v[130:133], v[122:125], v[98:113]
	v_mfma_f32_32x32x16_bf16 v[66:81], v[134:137], v[122:125], v[66:81]
	ds_read_b128 v[130:133], v168
	ds_read_b128 v[134:137], v168 offset:4096
	v_add_f32_e32 v180, v90, v180
	v_add_f32_e32 v180, v91, v180
	v_add_f32_e32 v180, v92, v180
	v_add_f32_e32 v180, v93, v180
	v_add_f32_e32 v180, v94, v180
	v_add_f32_e32 v180, v95, v180
	v_add_f32_e32 v180, v96, v180
	v_add_f32_e32 v180, v97, v180
	s_waitcnt lgkmcnt(0)
	v_mfma_f32_32x32x16_bf16 v[98:113], v[130:133], v[126:129], v[98:113]
	v_mfma_f32_32x32x16_bf16 v[66:81], v[134:137], v[126:129], v[66:81]
	v_add_f32_e32 v172, v172, v180
	v_cvt_pk_bf16_f32 v130, v197, v200
	v_cvt_pk_bf16_f32 v131, v198, v202
	v_cvt_pk_bf16_f32 v132, v204, v207
	v_cvt_pk_bf16_f32 v133, v205, v210
	v_cvt_pk_bf16_f32 v134, v199, v203
	v_cvt_pk_bf16_f32 v135, v201, v209
	v_cvt_pk_bf16_f32 v136, v206, v211
	v_cvt_pk_bf16_f32 v137, v208, v212
	v_cvt_pk_bf16_f32 v138, v82, v83
	v_cvt_pk_bf16_f32 v139, v84, v85
	v_cvt_pk_bf16_f32 v140, v86, v87
	v_cvt_pk_bf16_f32 v141, v88, v89
	v_cvt_pk_bf16_f32 v142, v90, v91
	v_cvt_pk_bf16_f32 v143, v92, v93
	v_cvt_pk_bf16_f32 v144, v94, v95
	v_cvt_pk_bf16_f32 v145, v96, v97
	ds_read_b64_tr_b16 v[174:175], v160 offset:0
	ds_read_b64_tr_b16 v[176:177], v160 offset:0x800
	ds_read_b64_tr_b16 v[184:185], v160 offset:0x1000
	ds_read_b64_tr_b16 v[186:187], v160 offset:0x1800
	ds_read_b64_tr_b16 v[188:189], v160 offset:0x2000
	ds_read_b64_tr_b16 v[190:191], v160 offset:0x2800
	ds_read_b64_tr_b16 v[192:193], v160 offset:0x3000
	ds_read_b64_tr_b16 v[194:195], v160 offset:0x3800
	ds_read_b64_tr_b16 v[214:215], v160 offset:0x200
	ds_read_b64_tr_b16 v[216:217], v160 offset:0xa00
	ds_read_b64_tr_b16 v[218:219], v160 offset:0x1200
	s_nop 0
	v_permlane32_swap_b32_e32 v130, v132
	v_permlane32_swap_b32_e32 v131, v133
	ds_read_b64_tr_b16 v[220:221], v160 offset:0x1a00
	ds_read_b64_tr_b16 v[222:223], v160 offset:0x2200
	ds_read_b64_tr_b16 v[224:225], v160 offset:0x2a00
	ds_read_b64_tr_b16 v[226:227], v160 offset:0x3200
	ds_read_b64_tr_b16 v[228:229], v160 offset:0x3a00
	s_waitcnt lgkmcnt(8)
	v_permlane32_swap_b32_e32 v134, v136
	s_nop 0
	v_mfma_f32_32x32x16_bf16 v[2:17], v[130:133], v[174:177], v[2:17]
	v_permlane32_swap_b32_e32 v135, v137
	v_permlane32_swap_b32_e32 v138, v140
	v_permlane32_swap_b32_e32 v139, v141
	ds_read_b64_tr_b16 v[174:175], v160 offset:0x400
	v_mfma_f32_32x32x16_bf16 v[2:17], v[134:137], v[184:187], v[2:17]
	v_permlane32_swap_b32_e32 v142, v144
	v_permlane32_swap_b32_e32 v143, v145
	ds_read_b64_tr_b16 v[176:177], v160 offset:0xc00
	ds_read_b64_tr_b16 v[184:185], v160 offset:0x1400
	ds_read_b64_tr_b16 v[186:187], v160 offset:0x1c00
	v_mfma_f32_32x32x16_bf16 v[2:17], v[138:141], v[188:191], v[2:17]
	ds_read_b64_tr_b16 v[188:189], v160 offset:0x2400
	ds_read_b64_tr_b16 v[190:191], v160 offset:0x2c00
	v_exp_f32_e32 v173, v98
	v_exp_f32_e32 v196, v113
	v_mfma_f32_32x32x16_bf16 v[2:17], v[142:145], v[192:195], v[2:17]
	ds_read_b64_tr_b16 v[192:193], v160 offset:0x3400
	ds_read_b64_tr_b16 v[194:195], v160 offset:0x3c00
	s_waitcnt lgkmcnt(8)
	s_nop 0
	v_mfma_f32_32x32x16_bf16 v[50:65], v[130:133], v[214:217], v[50:65]
	ds_read_b64_tr_b16 v[214:215], v160 offset:0x600
	ds_read_b64_tr_b16 v[216:217], v160 offset:0xe00
	v_mfma_f32_32x32x16_bf16 v[50:65], v[134:137], v[218:221], v[50:65]
	ds_read_b64_tr_b16 v[218:219], v160 offset:0x1600
	ds_read_b64_tr_b16 v[220:221], v160 offset:0x1e00
	v_mfma_f32_32x32x16_bf16 v[50:65], v[138:141], v[222:225], v[50:65]
	ds_read_b64_tr_b16 v[222:223], v160 offset:0x2600
	ds_read_b64_tr_b16 v[224:225], v160 offset:0x2e00
	v_mfma_f32_32x32x16_bf16 v[50:65], v[142:145], v[226:229], v[50:65]
	ds_read_b64_tr_b16 v[226:227], v160 offset:0x3600
	ds_read_b64_tr_b16 v[228:229], v160 offset:0x3e00
	s_waitcnt lgkmcnt(8)
	s_nop 0
	s_waitcnt lgkmcnt(0)
	v_mfma_f32_32x32x16_bf16 v[34:49], v[130:133], v[174:177], v[34:49]
	v_exp_f32_e32 v174, v99
	v_exp_f32_e32 v175, v100
	v_mfma_f32_32x32x16_bf16 v[18:33], v[130:133], v[214:217], v[18:33]
	v_mfma_f32_32x32x16_bf16 v[34:49], v[134:137], v[184:187], v[34:49]
	v_exp_f32_e32 v184, v101
	v_exp_f32_e32 v185, v102
	v_exp_f32_e32 v186, v103
	v_exp_f32_e32 v187, v104
	v_mfma_f32_32x32x16_bf16 v[18:33], v[134:137], v[218:221], v[18:33]
	v_mfma_f32_32x32x16_bf16 v[34:49], v[138:141], v[188:191], v[34:49]
	v_exp_f32_e32 v188, v105
	v_exp_f32_e32 v189, v106
	v_exp_f32_e32 v190, v107
	v_exp_f32_e32 v191, v108
	v_mfma_f32_32x32x16_bf16 v[18:33], v[138:141], v[222:225], v[18:33]
	v_mfma_f32_32x32x16_bf16 v[34:49], v[142:145], v[192:195], v[34:49]
	v_exp_f32_e32 v192, v109
	v_exp_f32_e32 v193, v110
	v_exp_f32_e32 v194, v111
	v_exp_f32_e32 v195, v112
	v_mfma_f32_32x32x16_bf16 v[18:33], v[142:145], v[226:229], v[18:33]
.LBB0_880:
	s_add_u32 s76, s76, 0x8000
	s_addc_u32 s77, s77, 0
	s_add_u32 s78, s78, 0x180000
	s_addc_u32 s79, s79, 0
	s_add_i32 s24, s55, 4
	s_add_i32 s25, s55, -1
	s_addk_i32 s2, 0x100
	s_add_u32 s60, s60, 0x8000
	s_addc_u32 s45, s45, 0
	s_mov_b64 s[26:27], 0x180000
	s_add_u32 s4, s4, 0x180000
	v_lshl_add_u64 v[152:153], v[152:153], 0, s[26:27]
	s_mov_b64 s[26:27], 0x8000
	s_addc_u32 s5, s5, 0
	v_lshl_add_u64 v[154:155], v[154:155], 0, s[26:27]
	s_cmp_ge_u32 s25, s95
	v_lshl_add_u64 v[156:157], v[156:157], 0, s[26:27]
	s_cbranch_scc1 .LBB0_918
	s_mov_b32 s55, s24
	s_branch .LBB0_842

; #define DMA_ITER(j, PN0, PN1, PO0, PO1, KS, VS, DS) do { \
;     DMA_WAIT((j) + 1 >= NT); __syncthreads(); if ((j) + 2 < NT) DMA_TILE((j) + 2, DS); \
;     qkt<DK>(PN0, PN1, K_lds + (KS) * SHM_K, qr, r32, hi); \
;     finishSM(PO0, PO1, l_reg, pa0, pa1, pa2, pa3); \
;     pv_all_pipe<DV>(o, vb0 + (VS) * SHM_V, pa0, pa1, pa2, pa3); partialSM<DK, OFF>(PN0, PN1, negMC); } while (0)
; template <int DK, int DV, bool OFF, class QLoader> ...
;     ...
;   if (wid >= 4) __builtin_amdgcn_s_setprio(1);
;   for (int j = 1; j < NT; j += 4) {
;     DMA_ITER(j, pB0, pB1, pA0, pA1, 1, 0, 3);
;     if (j + 1 < NT) DMA_ITER(j + 1, pA0, pA1, pB0, pB1, 2, 1, 0);
;     if (j + 2 < NT) DMA_ITER(j + 2, pB0, pB1, pA0, pA1, 3, 2, 1);
;     if (j + 3 < NT) DMA_ITER(j + 3, pA0, pA1, pB0, pB1, 0, 3, 2);
;   }
.LBB0_1430:
	s_and_b64 vcc, exec, s[36:37]
	s_cbranch_vccnz .LBB0_1497
	v_add3_u32 v0, v154, v155, v156
	v_lshlrev_b32_e32 v34, 6, v153
	v_readlane_b32 s92, v251, 4
	s_add_i32 s45, s89, -1
	v_lshl_add_u32 v0, v0, 7, v34
	v_readlane_b32 s94, v251, 6
	v_or_b32_e32 v0, v0, v157
	v_lshlrev_b32_e32 v34, 7, v152
	v_readlane_b32 s95, v251, 7
	s_add_u32 s0, s94, s80
	v_sub_u32_e32 v0, v0, v34
	s_addc_u32 s1, s95, s79
	s_mulk_i32 s38, 0x600
	v_lshl_add_u64 v[90:91], s[0:1], 0, v[0:1]
	v_or_b32_e32 v0, s38, v151
	s_movk_i32 s0, 0xc0
	v_mad_u32_u24 v0, v149, s0, v0
	s_add_u32 s0, s94, s78
	s_addc_u32 s1, s95, s2
	v_mul_u32_u24_e32 v34, 0xc0, v149
	v_lshl_add_u64 v[92:93], s[0:1], 0, v[0:1]
	v_or_b32_e32 v0, s38, v150
	s_movk_i32 s38, 0x300
	v_add3_u32 v0, v0, v34, s38
	v_lshl_add_u64 v[94:95], s[0:1], 0, v[0:1]
	s_mov_b32 s92, 5
	v_readlane_b32 s93, v251, 12
	s_lshr_b32 s93, s93, 8
	s_branch .LBB0_1434
.LBB0_1432:
	ds_read_b128 v[50:53], v126 offset:32768
	ds_read_b128 v[54:57], v126 offset:40960
	ds_read_b128 v[82:85], v127 offset:32768
	ds_read_b128 v[86:89], v127 offset:40960
	v_exp_f32_e32 v34, v34
	v_exp_f32_e32 v35, v35
	s_waitcnt lgkmcnt(0)
	v_mfma_f32_32x32x16_bf16 v[66:81], v[50:53], v[98:101], 0
	v_exp_f32_e32 v36, v36
	v_exp_f32_e32 v37, v37
	v_exp_f32_e32 v38, v38
	v_exp_f32_e32 v39, v39
	v_exp_f32_e32 v40, v40
	v_exp_f32_e32 v41, v41
	v_exp_f32_e32 v42, v42
	v_mfma_f32_32x32x16_bf16 v[50:65], v[54:57], v[98:101], 0
	v_exp_f32_e32 v43, v43
	v_exp_f32_e32 v44, v44
	v_exp_f32_e32 v45, v45
	v_exp_f32_e32 v46, v46
	v_exp_f32_e32 v47, v47
	v_exp_f32_e32 v48, v48
	v_exp_f32_e32 v49, v49
	v_mfma_f32_32x32x16_bf16 v[66:81], v[82:85], v[102:105], v[66:81]
	v_add_f32_e32 v0, 0, v184
	v_add_f32_e32 v0, v186, v0
	v_add_f32_e32 v0, v185, v0
	v_add_f32_e32 v0, v187, v0
	v_add_f32_e32 v0, v189, v0
	v_add_f32_e32 v0, v193, v0
	v_add_f32_e32 v0, v192, v0
	v_mfma_f32_32x32x16_bf16 v[50:65], v[86:89], v[102:105], v[50:65]
	s_cmp_eq_u32 s93, 0
	s_cbranch_scc1 .Lmstag_4
	s_add_i32 s32, s92, 5
	s_cmp_ge_u32 s32, s89
	s_cbranch_scc1 .Lmstag_4
	v_lshl_add_u64 v[240:241], v[92:93], 0, s[12:13]
	s_mov_b64 s[96:97], 0x2a81e000
	v_lshl_add_u64 v[240:241], v[240:241], 0, s[96:97]
	s_add_i32 m0, s81, 0x8000
	s_nop 0
	global_load_lds_dwordx4 v[240:241], off
	v_lshl_add_u64 v[240:241], v[94:95], 0, s[12:13]
	v_lshl_add_u64 v[240:241], v[240:241], 0, s[96:97]
	s_add_i32 m0, s81, 0x8400
	s_mov_b64 s[96:97], 0x30e14000
	global_load_lds_dwordx4 v[240:241], off
	v_lshl_add_u64 v[240:241], v[90:91], 0, s[12:13]
	v_lshl_add_u64 v[240:241], v[240:241], 0, s[96:97]
	s_add_i32 m0, s87, 0x4000
	s_nop 0
	global_load_lds_dwordx4 v[240:241], off
.Lmstag_4:
	ds_read_b128 v[82:85], v128 offset:32768
	ds_read_b128 v[86:89], v128 offset:40960
	v_add_f32_e32 v0, v194, v0
	v_add_f32_e32 v0, v188, v0
	v_add_f32_e32 v0, v191, v0
	v_add_f32_e32 v0, v190, v0
	v_add_f32_e32 v0, v196, v0
	v_add_f32_e32 v0, v195, v0
	s_waitcnt lgkmcnt(0)
	v_mfma_f32_32x32x16_bf16 v[66:81], v[82:85], v[106:109], v[66:81]
	v_add_f32_e32 v0, v198, v0
	v_add_f32_e32 v0, v197, v0
	v_add_f32_e32 v0, v199, v0
	v_add_f32_e32 v0, v34, v0
	v_add_f32_e32 v0, v35, v0
	v_add_f32_e32 v0, v36, v0
	v_add_f32_e32 v0, v37, v0
	v_mfma_f32_32x32x16_bf16 v[50:65], v[86:89], v[106:109], v[50:65]
	ds_read_b128 v[82:85], v129 offset:32768
	ds_read_b128 v[86:89], v129 offset:40960
	v_add_f32_e32 v0, v38, v0
	v_add_f32_e32 v0, v39, v0
	v_add_f32_e32 v0, v40, v0
	v_add_f32_e32 v0, v41, v0
	v_add_f32_e32 v0, v42, v0
	v_add_f32_e32 v0, v43, v0
	s_waitcnt lgkmcnt(0)
	v_mfma_f32_32x32x16_bf16 v[66:81], v[82:85], v[110:113], v[66:81]
	v_add_f32_e32 v0, v44, v0
	v_add_f32_e32 v0, v45, v0
	v_add_f32_e32 v0, v46, v0
	v_add_f32_e32 v0, v47, v0
	v_add_f32_e32 v0, v48, v0
	v_add_f32_e32 v0, v49, v0
	v_add_f32_e32 v145, v145, v0
	v_mfma_f32_32x32x16_bf16 v[50:65], v[86:89], v[110:113], v[50:65]
	ds_read_b128 v[82:85], v130 offset:32768
	ds_read_b128 v[86:89], v130 offset:40960
	s_waitcnt lgkmcnt(0)
	v_mfma_f32_32x32x16_bf16 v[66:81], v[82:85], v[114:117], v[66:81]
	v_mfma_f32_32x32x16_bf16 v[50:65], v[86:89], v[114:117], v[50:65]
	ds_read_b128 v[82:85], v131 offset:32768
	ds_read_b128 v[86:89], v131 offset:40960
	s_waitcnt lgkmcnt(0)
	v_mfma_f32_32x32x16_bf16 v[66:81], v[82:85], v[118:121], v[66:81]
	v_cvt_pk_bf16_f32 v82, v184, v186
	v_cvt_pk_bf16_f32 v83, v185, v187
	v_cvt_pk_bf16_f32 v84, v189, v193
	v_cvt_pk_bf16_f32 v85, v192, v194
	s_nop 0
	v_permlane32_swap_b32_e32 v82, v84
	v_mfma_f32_32x32x16_bf16 v[50:65], v[86:89], v[118:121], v[50:65]
	v_cvt_pk_bf16_f32 v86, v188, v191
	v_cvt_pk_bf16_f32 v87, v190, v196
	v_cvt_pk_bf16_f32 v88, v195, v198
	v_cvt_pk_bf16_f32 v89, v197, v199
	v_cvt_pk_bf16_f32 v122, v34, v35
	v_cvt_pk_bf16_f32 v123, v36, v37
	v_cvt_pk_bf16_f32 v124, v38, v39
	v_cvt_pk_bf16_f32 v125, v40, v41
	v_cvt_pk_bf16_f32 v150, v42, v43
	v_cvt_pk_bf16_f32 v151, v44, v45
	v_cvt_pk_bf16_f32 v152, v46, v47
	v_cvt_pk_bf16_f32 v153, v48, v49
	ds_read_b64_tr_b16 v[154:155], v96 offset:0
	ds_read_b64_tr_b16 v[156:157], v96 offset:0x400
	ds_read_b64_tr_b16 v[158:159], v96 offset:0x800
	ds_read_b64_tr_b16 v[160:161], v96 offset:0xc00
	ds_read_b64_tr_b16 v[162:163], v96 offset:0x1000
	ds_read_b64_tr_b16 v[164:165], v96 offset:0x1400
	ds_read_b64_tr_b16 v[166:167], v96 offset:0x1800
	ds_read_b64_tr_b16 v[168:169], v96 offset:0x1c00
	ds_read_b64_tr_b16 v[170:171], v96 offset:0x200
	ds_read_b64_tr_b16 v[172:173], v96 offset:0x600
	ds_read_b64_tr_b16 v[200:201], v96 offset:0xa00
	ds_read_b64_tr_b16 v[202:203], v96 offset:0xe00
	v_permlane32_swap_b32_e32 v83, v85
	ds_read_b64_tr_b16 v[204:205], v96 offset:0x1200
	ds_read_b64_tr_b16 v[206:207], v96 offset:0x1600
	ds_read_b64_tr_b16 v[208:209], v96 offset:0x1a00
	ds_read_b64_tr_b16 v[210:211], v96 offset:0x1e00
	s_waitcnt lgkmcnt(8)
	v_permlane32_swap_b32_e32 v86, v88
	s_nop 0
	v_mfma_f32_32x32x16_bf16 v[2:17], v[82:85], v[154:157], v[2:17]
	s_waitcnt lgkmcnt(0)
	v_permlane32_swap_b32_e32 v87, v89
	v_permlane32_swap_b32_e32 v122, v124
	v_permlane32_swap_b32_e32 v123, v125
	v_mfma_f32_32x32x16_bf16 v[18:33], v[82:85], v[170:173], v[18:33]
	v_permlane32_swap_b32_e32 v150, v152
	v_permlane32_swap_b32_e32 v151, v153
	v_exp_f32_e32 v170, v76
	v_exp_f32_e32 v171, v77
	v_exp_f32_e32 v172, v78
	v_mfma_f32_32x32x16_bf16 v[2:17], v[86:89], v[158:161], v[2:17]
	v_exp_f32_e32 v158, v66
	v_exp_f32_e32 v159, v67
	v_exp_f32_e32 v160, v68
	v_exp_f32_e32 v161, v69
	v_exp_f32_e32 v173, v79
	v_exp_f32_e32 v174, v80
	v_exp_f32_e32 v175, v81
	v_mfma_f32_32x32x16_bf16 v[18:33], v[86:89], v[200:203], v[18:33]
	v_mfma_f32_32x32x16_bf16 v[2:17], v[122:125], v[162:165], v[2:17]
	v_exp_f32_e32 v162, v70
	v_exp_f32_e32 v163, v71
	v_mfma_f32_32x32x16_bf16 v[18:33], v[122:125], v[204:207], v[18:33]
	v_mfma_f32_32x32x16_bf16 v[2:17], v[150:153], v[166:169], v[2:17]
	v_exp_f32_e32 v166, v72
	v_exp_f32_e32 v167, v73
	v_exp_f32_e32 v168, v74
	v_exp_f32_e32 v169, v75
	v_mfma_f32_32x32x16_bf16 v[18:33], v[150:153], v[208:211], v[18:33]

; #define DMA_WAIT(last) do { if (last) asm volatile("s_waitcnt vmcnt(0)" ::: "memory"); else asm volatile("s_waitcnt vmcnt(%0)" :: "n"(NPW) : "memory"); } while (0)
; template <int DK>
; __device__ __forceinline__ void qkt(f32x16& p0, f32x16& p1, const char* Ks, const bf16x8* qr, int r32, int hi) {
;   p0 = f32x16{}; p1 = f32x16{};
; #pragma unroll
;   for (int d0 = 0; d0 < DK / 16; ++d0) { const int cb = (d0 * 16 + hi * 8) * 2;
;     const bf16x8 b0 = *reinterpret_cast<const bf16x8*>(Ks + ATT_KSWZ(r32, cb));
;     const bf16x8 b1 = *reinterpret_cast<const bf16x8*>(Ks + ATT_KSWZ(32 + r32, cb));
;     p0 = __builtin_amdgcn_mfma_f32_32x32x16_bf16(b0, qr[d0], p0, 0, 0, 0);
;     p1 = __builtin_amdgcn_mfma_f32_32x32x16_bf16(b1, qr[d0], p1, 0, 0, 0);
;   }
; }
; template <int DK, int DV, bool OFF, class QLoader> ...
;     ...
;   f32x16 pA0, pA1, pB0, pB1; bf16x8 pa0, pa1, pa2, pa3; const int NT = nkeys / KVBLK;
;   DMA_TILE(0, 0); DMA_TILE(1, 1); DMA_WAIT(false); __syncthreads(); if (2 < NT) DMA_TILE(2, 2);
;   qkt<DK>(pA0, pA1, K_lds, qr, r32, hi); partialSM<DK, OFF>(pA0, pA1, negMC);
.LBB0_1436:
.LBB0_1438:
	s_add_i32 s40, s92, 2
	s_cmp_lt_u32 s40, s89
	s_cselect_b64 s[0:1], -1, 0
	s_cmp_ge_u32 s40, s89
	s_cselect_b64 s[40:41], -1, 0
	s_and_b64 vcc, exec, s[40:41]
	s_waitcnt vmcnt(0)
	s_barrier
	s_cbranch_vccnz .LBB0_1440
	s_cmp_lg_u32 s93, 0
	s_cbranch_scc1 .LBB0_1440
	v_lshl_add_u64 v[34:35], v[92:93], 0, s[12:13]
	s_mov_b64 s[94:95], 0x2a815000
	s_mov_b32 m0, s85
	v_lshl_add_u64 v[34:35], v[34:35], 0, s[94:95]
	global_load_lds_dwordx4 v[34:35], off
	v_lshl_add_u64 v[34:35], v[94:95], 0, s[12:13]
	v_lshl_add_u64 v[34:35], v[34:35], 0, s[94:95]
	s_mov_b32 m0, s86
	s_mov_b64 s[94:95], 0x30e0e000
	global_load_lds_dwordx4 v[34:35], off
	v_lshl_add_u64 v[34:35], v[90:91], 0, s[12:13]
	v_lshl_add_u64 v[34:35], v[34:35], 0, s[94:95]
	s_mov_b32 m0, s88
	s_nop 0
	global_load_lds_dwordx4 v[34:35], off
.LBB0_1440:
	ds_read_b128 v[34:37], v126 offset:49152
	ds_read_b128 v[38:41], v126 offset:57344
	ds_read_b128 v[82:85], v127 offset:49152
	ds_read_b128 v[86:89], v127 offset:57344
	v_exp_f32_e32 v50, v50
	v_exp_f32_e32 v51, v51
	s_waitcnt lgkmcnt(0)
	v_mfma_f32_32x32x16_bf16 v[66:81], v[34:37], v[98:101], 0
	v_exp_f32_e32 v52, v52
	v_exp_f32_e32 v53, v53
	v_exp_f32_e32 v54, v54
	v_exp_f32_e32 v55, v55
	v_exp_f32_e32 v56, v56
	v_exp_f32_e32 v57, v57
	v_exp_f32_e32 v58, v58
	v_mfma_f32_32x32x16_bf16 v[34:49], v[38:41], v[98:101], 0
	v_exp_f32_e32 v59, v59
	v_exp_f32_e32 v60, v60
	v_exp_f32_e32 v61, v61
	v_exp_f32_e32 v62, v62
	v_exp_f32_e32 v63, v63
	v_exp_f32_e32 v64, v64
	v_exp_f32_e32 v65, v65
	v_mfma_f32_32x32x16_bf16 v[66:81], v[82:85], v[102:105], v[66:81]
	v_add_f32_e32 v0, 0, v158
	v_add_f32_e32 v0, v159, v0
	v_add_f32_e32 v0, v160, v0
	v_add_f32_e32 v0, v161, v0
	v_add_f32_e32 v0, v162, v0
	v_add_f32_e32 v0, v163, v0
	v_add_f32_e32 v0, v166, v0
	v_mfma_f32_32x32x16_bf16 v[34:49], v[86:89], v[102:105], v[34:49]
	s_cmp_eq_u32 s93, 0
	s_cbranch_scc1 .Lmstag_1
	s_add_i32 s32, s92, 2
	s_cmp_ge_u32 s32, s89
	s_cbranch_scc1 .Lmstag_1
	v_lshl_add_u64 v[240:241], v[92:93], 0, s[12:13]
	s_mov_b64 s[96:97], 0x2a815000
	s_mov_b32 m0, s85
	v_lshl_add_u64 v[240:241], v[240:241], 0, s[96:97]
	global_load_lds_dwordx4 v[240:241], off
	v_lshl_add_u64 v[240:241], v[94:95], 0, s[12:13]
	v_lshl_add_u64 v[240:241], v[240:241], 0, s[96:97]
	s_mov_b32 m0, s86
	s_mov_b64 s[96:97], 0x30e0e000
	global_load_lds_dwordx4 v[240:241], off
	v_lshl_add_u64 v[240:241], v[90:91], 0, s[12:13]
	v_lshl_add_u64 v[240:241], v[240:241], 0, s[96:97]
	s_mov_b32 m0, s88
	s_nop 0
	global_load_lds_dwordx4 v[240:241], off
.Lmstag_1:
	ds_read_b128 v[82:85], v128 offset:49152
	ds_read_b128 v[86:89], v128 offset:57344
	v_add_f32_e32 v0, v167, v0
	v_add_f32_e32 v0, v168, v0
	v_add_f32_e32 v0, v169, v0
	v_add_f32_e32 v0, v170, v0
	v_add_f32_e32 v0, v171, v0
	v_add_f32_e32 v0, v172, v0
	s_waitcnt lgkmcnt(0)
	v_mfma_f32_32x32x16_bf16 v[66:81], v[82:85], v[106:109], v[66:81]
	v_add_f32_e32 v0, v173, v0
	v_add_f32_e32 v0, v174, v0
	v_add_f32_e32 v0, v175, v0
	v_add_f32_e32 v0, v50, v0
	v_add_f32_e32 v0, v51, v0
	v_add_f32_e32 v0, v52, v0
	v_add_f32_e32 v0, v53, v0
	v_mfma_f32_32x32x16_bf16 v[34:49], v[86:89], v[106:109], v[34:49]
	ds_read_b128 v[82:85], v129 offset:49152
	ds_read_b128 v[86:89], v129 offset:57344
	v_add_f32_e32 v0, v54, v0
	v_add_f32_e32 v0, v55, v0
	v_add_f32_e32 v0, v56, v0
	v_add_f32_e32 v0, v57, v0
	v_add_f32_e32 v0, v58, v0
	v_add_f32_e32 v0, v59, v0
	s_waitcnt lgkmcnt(0)
	v_mfma_f32_32x32x16_bf16 v[66:81], v[82:85], v[110:113], v[66:81]
	v_add_f32_e32 v0, v60, v0
	v_add_f32_e32 v0, v61, v0
	v_add_f32_e32 v0, v62, v0
	v_add_f32_e32 v0, v63, v0
	v_add_f32_e32 v0, v64, v0
	v_add_f32_e32 v0, v65, v0
	v_add_f32_e32 v145, v145, v0
	v_mfma_f32_32x32x16_bf16 v[34:49], v[86:89], v[110:113], v[34:49]
	ds_read_b128 v[82:85], v130 offset:49152
	ds_read_b128 v[86:89], v130 offset:57344
	s_andn2_b64 vcc, exec, s[38:39]
	s_waitcnt lgkmcnt(0)
	v_mfma_f32_32x32x16_bf16 v[66:81], v[82:85], v[114:117], v[66:81]
	v_mfma_f32_32x32x16_bf16 v[34:49], v[86:89], v[114:117], v[34:49]
	ds_read_b128 v[82:85], v131 offset:49152
	ds_read_b128 v[86:89], v131 offset:57344
	s_waitcnt lgkmcnt(0)
	v_mfma_f32_32x32x16_bf16 v[66:81], v[82:85], v[118:121], v[66:81]
	v_cvt_pk_bf16_f32 v82, v158, v159
	v_cvt_pk_bf16_f32 v83, v160, v161
	v_cvt_pk_bf16_f32 v84, v162, v163
	v_cvt_pk_bf16_f32 v85, v166, v167
	s_nop 0
	v_permlane32_swap_b32_e32 v82, v84
	v_mfma_f32_32x32x16_bf16 v[34:49], v[86:89], v[118:121], v[34:49]
	v_cvt_pk_bf16_f32 v86, v168, v169
	v_cvt_pk_bf16_f32 v87, v170, v171
	v_cvt_pk_bf16_f32 v88, v172, v173
	v_cvt_pk_bf16_f32 v89, v174, v175
	v_cvt_pk_bf16_f32 v122, v50, v51
	v_cvt_pk_bf16_f32 v123, v52, v53
	v_cvt_pk_bf16_f32 v124, v54, v55
	v_cvt_pk_bf16_f32 v125, v56, v57
	v_cvt_pk_bf16_f32 v150, v58, v59
	v_cvt_pk_bf16_f32 v151, v60, v61
	v_cvt_pk_bf16_f32 v152, v62, v63
	v_cvt_pk_bf16_f32 v153, v64, v65
	ds_read_b64_tr_b16 v[154:155], v132 offset:0
	ds_read_b64_tr_b16 v[156:157], v132 offset:0x400
	ds_read_b64_tr_b16 v[184:185], v132 offset:0x800
	ds_read_b64_tr_b16 v[186:187], v132 offset:0xc00
	ds_read_b64_tr_b16 v[188:189], v132 offset:0x1000
	ds_read_b64_tr_b16 v[190:191], v132 offset:0x1400
	ds_read_b64_tr_b16 v[192:193], v132 offset:0x1800
	ds_read_b64_tr_b16 v[194:195], v132 offset:0x1c00
	ds_read_b64_tr_b16 v[196:197], v132 offset:0x200
	ds_read_b64_tr_b16 v[198:199], v132 offset:0x600
	ds_read_b64_tr_b16 v[200:201], v132 offset:0xa00
	ds_read_b64_tr_b16 v[202:203], v132 offset:0xe00
	v_permlane32_swap_b32_e32 v83, v85
	ds_read_b64_tr_b16 v[204:205], v132 offset:0x1200
	ds_read_b64_tr_b16 v[206:207], v132 offset:0x1600
	ds_read_b64_tr_b16 v[208:209], v132 offset:0x1a00
	ds_read_b64_tr_b16 v[210:211], v132 offset:0x1e00
	s_waitcnt lgkmcnt(8)
	v_permlane32_swap_b32_e32 v86, v88
	s_nop 0
	v_mfma_f32_32x32x16_bf16 v[2:17], v[82:85], v[154:157], v[2:17]
	s_waitcnt lgkmcnt(0)
	v_permlane32_swap_b32_e32 v87, v89
	v_permlane32_swap_b32_e32 v122, v124
	v_permlane32_swap_b32_e32 v123, v125
	v_mfma_f32_32x32x16_bf16 v[18:33], v[82:85], v[196:199], v[18:33]
	v_permlane32_swap_b32_e32 v150, v152
	v_permlane32_swap_b32_e32 v151, v153
	v_exp_f32_e32 v196, v77
	v_exp_f32_e32 v198, v79
	v_exp_f32_e32 v197, v80
	v_mfma_f32_32x32x16_bf16 v[2:17], v[86:89], v[184:187], v[2:17]
	v_exp_f32_e32 v184, v66
	v_exp_f32_e32 v186, v67
	v_exp_f32_e32 v185, v68
	v_exp_f32_e32 v187, v69
	v_exp_f32_e32 v199, v81
	v_mfma_f32_32x32x16_bf16 v[18:33], v[86:89], v[200:203], v[18:33]
	v_mfma_f32_32x32x16_bf16 v[2:17], v[122:125], v[188:191], v[2:17]
	v_exp_f32_e32 v189, v70
	v_exp_f32_e32 v188, v74
	v_exp_f32_e32 v191, v75
	v_exp_f32_e32 v190, v76
	v_mfma_f32_32x32x16_bf16 v[18:33], v[122:125], v[204:207], v[18:33]
	v_mfma_f32_32x32x16_bf16 v[2:17], v[150:153], v[192:195], v[2:17]
	v_exp_f32_e32 v193, v71
	v_exp_f32_e32 v192, v72
	v_exp_f32_e32 v194, v73
	v_exp_f32_e32 v195, v78
	v_mfma_f32_32x32x16_bf16 v[18:33], v[150:153], v[208:211], v[18:33]
	s_cbranch_vccnz .LBB0_1449
; #define DMA_WAIT(last) do { if (last) asm volatile("s_waitcnt vmcnt(0)" ::: "memory"); else asm volatile("s_waitcnt vmcnt(%0)" :: "n"(NPW) : "memory"); } while (0)
; template <int DK>
; __device__ __forceinline__ void qkt(f32x16& p0, f32x16& p1, const char* Ks, const bf16x8* qr, int r32, int hi) {
;   p0 = f32x16{}; p1 = f32x16{};
; #pragma unroll
;   for (int d0 = 0; d0 < DK / 16; ++d0) { const int cb = (d0 * 16 + hi * 8) * 2;
;     const bf16x8 b0 = *reinterpret_cast<const bf16x8*>(Ks + ATT_KSWZ(r32, cb));
;     const bf16x8 b1 = *reinterpret_cast<const bf16x8*>(Ks + ATT_KSWZ(32 + r32, cb));
;     p0 = __builtin_amdgcn_mfma_f32_32x32x16_bf16(b0, qr[d0], p0, 0, 0, 0);
;     p1 = __builtin_amdgcn_mfma_f32_32x32x16_bf16(b1, qr[d0], p1, 0, 0, 0);
;   }
; }
; template <int DK, int DV, bool OFF, class QLoader> ...
;     ...
;   f32x16 pA0, pA1, pB0, pB1; bf16x8 pa0, pa1, pa2, pa3; const int NT = nkeys / KVBLK;
;   DMA_TILE(0, 0); DMA_TILE(1, 1); DMA_WAIT(false); __syncthreads(); if (2 < NT) DMA_TILE(2, 2);
;   qkt<DK>(pA0, pA1, K_lds, qr, r32, hi); partialSM<DK, OFF>(pA0, pA1, negMC);
.LBB0_1443:
.LBB0_1445:
	s_add_i32 s38, s92, 3
	s_cmp_ge_u32 s38, s89
	s_waitcnt vmcnt(0)
	s_barrier
	s_cbranch_scc1 .LBB0_1447
	s_cmp_lg_u32 s93, 0
	s_cbranch_scc1 .LBB0_1447
	v_lshl_add_u64 v[50:51], v[92:93], 0, s[12:13]
	s_mov_b64 s[38:39], 0x2a818000
	s_mov_b32 m0, s81
	v_lshl_add_u64 v[50:51], v[50:51], 0, s[38:39]
	global_load_lds_dwordx4 v[50:51], off
	v_lshl_add_u64 v[50:51], v[94:95], 0, s[12:13]
	v_lshl_add_u64 v[50:51], v[50:51], 0, s[38:39]
	s_mov_b32 m0, s82
	s_mov_b64 s[38:39], 0x30e10000
	global_load_lds_dwordx4 v[50:51], off
	v_lshl_add_u64 v[50:51], v[90:91], 0, s[12:13]
	v_lshl_add_u64 v[50:51], v[50:51], 0, s[38:39]
	s_mov_b32 m0, s87
	s_nop 0
	global_load_lds_dwordx4 v[50:51], off
.LBB0_1447:
	ds_read_b128 v[50:53], v133
	ds_read_b128 v[54:57], v133 offset:8192
	ds_read_b128 v[82:85], v134
	ds_read_b128 v[86:89], v134 offset:8192
	v_exp_f32_e32 v34, v34
	v_exp_f32_e32 v35, v35
	s_waitcnt lgkmcnt(0)
	v_mfma_f32_32x32x16_bf16 v[66:81], v[50:53], v[98:101], 0
	v_exp_f32_e32 v36, v36
	v_exp_f32_e32 v37, v37
	v_exp_f32_e32 v38, v38
	v_exp_f32_e32 v39, v39
	v_exp_f32_e32 v40, v40
	v_exp_f32_e32 v41, v41
	v_exp_f32_e32 v42, v42
	v_mfma_f32_32x32x16_bf16 v[50:65], v[54:57], v[98:101], 0
	v_exp_f32_e32 v43, v43
	v_exp_f32_e32 v44, v44
	v_exp_f32_e32 v45, v45
	v_exp_f32_e32 v46, v46
	v_exp_f32_e32 v47, v47
	v_exp_f32_e32 v48, v48
	v_exp_f32_e32 v49, v49
	v_mfma_f32_32x32x16_bf16 v[66:81], v[82:85], v[102:105], v[66:81]
	v_add_f32_e32 v0, 0, v184
	v_add_f32_e32 v0, v186, v0
	v_add_f32_e32 v0, v185, v0
	v_add_f32_e32 v0, v187, v0
	v_add_f32_e32 v0, v189, v0
	v_add_f32_e32 v0, v193, v0
	v_add_f32_e32 v0, v192, v0
	v_mfma_f32_32x32x16_bf16 v[50:65], v[86:89], v[102:105], v[50:65]
	s_cmp_eq_u32 s93, 0
	s_cbranch_scc1 .Lmstag_2
	s_add_i32 s32, s92, 3
	s_cmp_ge_u32 s32, s89
	s_cbranch_scc1 .Lmstag_2
	v_lshl_add_u64 v[240:241], v[92:93], 0, s[12:13]
	s_mov_b64 s[96:97], 0x2a818000
	s_mov_b32 m0, s81
	v_lshl_add_u64 v[240:241], v[240:241], 0, s[96:97]
	global_load_lds_dwordx4 v[240:241], off
	v_lshl_add_u64 v[240:241], v[94:95], 0, s[12:13]
	v_lshl_add_u64 v[240:241], v[240:241], 0, s[96:97]
	s_mov_b32 m0, s82
	s_mov_b64 s[96:97], 0x30e10000
	global_load_lds_dwordx4 v[240:241], off
	v_lshl_add_u64 v[240:241], v[90:91], 0, s[12:13]
	v_lshl_add_u64 v[240:241], v[240:241], 0, s[96:97]
	s_mov_b32 m0, s87
	s_nop 0
	global_load_lds_dwordx4 v[240:241], off
.Lmstag_2:
	ds_read_b128 v[82:85], v135
	ds_read_b128 v[86:89], v135 offset:8192
	v_add_f32_e32 v0, v194, v0
	v_add_f32_e32 v0, v188, v0
	v_add_f32_e32 v0, v191, v0
	v_add_f32_e32 v0, v190, v0
	v_add_f32_e32 v0, v196, v0
	v_add_f32_e32 v0, v195, v0
	s_waitcnt lgkmcnt(0)
	v_mfma_f32_32x32x16_bf16 v[66:81], v[82:85], v[106:109], v[66:81]
	v_add_f32_e32 v0, v198, v0
	v_add_f32_e32 v0, v197, v0
	v_add_f32_e32 v0, v199, v0
	v_add_f32_e32 v0, v34, v0
	v_add_f32_e32 v0, v35, v0
	v_add_f32_e32 v0, v36, v0
	v_add_f32_e32 v0, v37, v0
	v_mfma_f32_32x32x16_bf16 v[50:65], v[86:89], v[106:109], v[50:65]
	ds_read_b128 v[82:85], v136
	ds_read_b128 v[86:89], v136 offset:8192
	v_add_f32_e32 v0, v38, v0
	v_add_f32_e32 v0, v39, v0
	v_add_f32_e32 v0, v40, v0
	v_add_f32_e32 v0, v41, v0
	v_add_f32_e32 v0, v42, v0
	v_add_f32_e32 v0, v43, v0
	s_waitcnt lgkmcnt(0)
	v_mfma_f32_32x32x16_bf16 v[66:81], v[82:85], v[110:113], v[66:81]
	v_add_f32_e32 v0, v44, v0
	v_add_f32_e32 v0, v45, v0
	v_add_f32_e32 v0, v46, v0
	v_add_f32_e32 v0, v47, v0
	v_add_f32_e32 v0, v48, v0
	v_add_f32_e32 v0, v49, v0
	v_add_f32_e32 v145, v145, v0
	v_mfma_f32_32x32x16_bf16 v[50:65], v[86:89], v[110:113], v[50:65]
	ds_read_b128 v[82:85], v137
	ds_read_b128 v[86:89], v137 offset:8192
	s_waitcnt lgkmcnt(0)
	v_mfma_f32_32x32x16_bf16 v[66:81], v[82:85], v[114:117], v[66:81]
	v_mfma_f32_32x32x16_bf16 v[50:65], v[86:89], v[114:117], v[50:65]
	ds_read_b128 v[82:85], v138
	ds_read_b128 v[86:89], v138 offset:8192
	s_waitcnt lgkmcnt(0)
	v_mfma_f32_32x32x16_bf16 v[66:81], v[82:85], v[118:121], v[66:81]
	v_cvt_pk_bf16_f32 v82, v184, v186
	v_cvt_pk_bf16_f32 v83, v185, v187
	v_cvt_pk_bf16_f32 v84, v189, v193
	v_cvt_pk_bf16_f32 v85, v192, v194
	s_nop 0
	v_permlane32_swap_b32_e32 v82, v84
	v_mfma_f32_32x32x16_bf16 v[50:65], v[86:89], v[118:121], v[50:65]
	v_cvt_pk_bf16_f32 v86, v188, v191
	v_cvt_pk_bf16_f32 v87, v190, v196
	v_cvt_pk_bf16_f32 v88, v195, v198
	v_cvt_pk_bf16_f32 v89, v197, v199
	v_cvt_pk_bf16_f32 v122, v34, v35
	v_cvt_pk_bf16_f32 v123, v36, v37
	v_cvt_pk_bf16_f32 v124, v38, v39
	v_cvt_pk_bf16_f32 v125, v40, v41
	v_cvt_pk_bf16_f32 v150, v42, v43
	v_cvt_pk_bf16_f32 v151, v44, v45
	v_cvt_pk_bf16_f32 v152, v46, v47
	v_cvt_pk_bf16_f32 v153, v48, v49
	ds_read_b64_tr_b16 v[154:155], v139 offset:0
	ds_read_b64_tr_b16 v[156:157], v139 offset:0x400
	ds_read_b64_tr_b16 v[158:159], v139 offset:0x800
	ds_read_b64_tr_b16 v[160:161], v139 offset:0xc00
	ds_read_b64_tr_b16 v[162:163], v139 offset:0x1000
	ds_read_b64_tr_b16 v[164:165], v139 offset:0x1400
	ds_read_b64_tr_b16 v[166:167], v139 offset:0x1800
	ds_read_b64_tr_b16 v[168:169], v139 offset:0x1c00
	ds_read_b64_tr_b16 v[170:171], v139 offset:0x200
	ds_read_b64_tr_b16 v[172:173], v139 offset:0x600
	ds_read_b64_tr_b16 v[200:201], v139 offset:0xa00
	ds_read_b64_tr_b16 v[202:203], v139 offset:0xe00
	v_permlane32_swap_b32_e32 v83, v85
	ds_read_b64_tr_b16 v[204:205], v139 offset:0x1200
	ds_read_b64_tr_b16 v[206:207], v139 offset:0x1600
	ds_read_b64_tr_b16 v[208:209], v139 offset:0x1a00
	ds_read_b64_tr_b16 v[210:211], v139 offset:0x1e00
	s_waitcnt lgkmcnt(8)
	v_permlane32_swap_b32_e32 v86, v88
	s_nop 0
	v_mfma_f32_32x32x16_bf16 v[2:17], v[82:85], v[154:157], v[2:17]
	s_waitcnt lgkmcnt(0)
	v_permlane32_swap_b32_e32 v87, v89
	v_permlane32_swap_b32_e32 v122, v124
	v_permlane32_swap_b32_e32 v123, v125
	v_mfma_f32_32x32x16_bf16 v[18:33], v[82:85], v[170:173], v[18:33]
	v_permlane32_swap_b32_e32 v150, v152
	v_permlane32_swap_b32_e32 v151, v153
	v_exp_f32_e32 v170, v76
	v_exp_f32_e32 v171, v77
	v_exp_f32_e32 v172, v78
	v_mfma_f32_32x32x16_bf16 v[2:17], v[86:89], v[158:161], v[2:17]
	v_exp_f32_e32 v158, v66
	v_exp_f32_e32 v159, v67
	v_exp_f32_e32 v160, v68
	v_exp_f32_e32 v161, v69
	v_exp_f32_e32 v173, v79
	v_exp_f32_e32 v174, v80
	v_exp_f32_e32 v175, v81
	v_mfma_f32_32x32x16_bf16 v[18:33], v[86:89], v[200:203], v[18:33]
	v_mfma_f32_32x32x16_bf16 v[2:17], v[122:125], v[162:165], v[2:17]
	v_exp_f32_e32 v162, v70
	v_exp_f32_e32 v163, v71
	v_mfma_f32_32x32x16_bf16 v[18:33], v[122:125], v[204:207], v[18:33]
	v_mfma_f32_32x32x16_bf16 v[2:17], v[150:153], v[166:169], v[2:17]
	v_exp_f32_e32 v166, v72
	v_exp_f32_e32 v167, v73
	v_exp_f32_e32 v168, v74
	v_exp_f32_e32 v169, v75
	v_mfma_f32_32x32x16_bf16 v[18:33], v[150:153], v[208:211], v[18:33]
	s_andn2_b64 vcc, exec, s[0:1]
	s_cbranch_vccz .LBB0_1450

; #define DMA_WAIT(last) do { if (last) asm volatile("s_waitcnt vmcnt(0)" ::: "memory"); else asm volatile("s_waitcnt vmcnt(%0)" :: "n"(NPW) : "memory"); } while (0)
; template <int DK>
; __device__ __forceinline__ void qkt(f32x16& p0, f32x16& p1, const char* Ks, const bf16x8* qr, int r32, int hi) {
;   p0 = f32x16{}; p1 = f32x16{};
; #pragma unroll
;   for (int d0 = 0; d0 < DK / 16; ++d0) { const int cb = (d0 * 16 + hi * 8) * 2;
;     const bf16x8 b0 = *reinterpret_cast<const bf16x8*>(Ks + ATT_KSWZ(r32, cb));
;     const bf16x8 b1 = *reinterpret_cast<const bf16x8*>(Ks + ATT_KSWZ(32 + r32, cb));
;     p0 = __builtin_amdgcn_mfma_f32_32x32x16_bf16(b0, qr[d0], p0, 0, 0, 0);
;     p1 = __builtin_amdgcn_mfma_f32_32x32x16_bf16(b1, qr[d0], p1, 0, 0, 0);
;   }
; }
; template <int DK, int DV, bool OFF, class QLoader> ...
;     ...
;   f32x16 pA0, pA1, pB0, pB1; bf16x8 pa0, pa1, pa2, pa3; const int NT = nkeys / KVBLK;
;   DMA_TILE(0, 0); DMA_TILE(1, 1); DMA_WAIT(false); __syncthreads(); if (2 < NT) DMA_TILE(2, 2);
;   qkt<DK>(pA0, pA1, K_lds, qr, r32, hi); partialSM<DK, OFF>(pA0, pA1, negMC);
.LBB0_1452:
.LBB0_1454:
	s_add_i32 s0, s92, 4
	s_cmp_ge_u32 s0, s89
	s_waitcnt vmcnt(0)
	s_barrier
	s_cbranch_scc1 .LBB0_1456
	s_cmp_lg_u32 s93, 0
	s_cbranch_scc1 .LBB0_1456
	v_lshl_add_u64 v[34:35], v[92:93], 0, s[12:13]
	s_mov_b64 s[0:1], 0x2a81b000
	s_mov_b32 m0, s83
	v_lshl_add_u64 v[34:35], v[34:35], 0, s[0:1]
	global_load_lds_dwordx4 v[34:35], off
	v_lshl_add_u64 v[34:35], v[94:95], 0, s[12:13]
	v_lshl_add_u64 v[34:35], v[34:35], 0, s[0:1]
	s_mov_b32 m0, s84
	s_mov_b64 s[0:1], 0x30e12000
	global_load_lds_dwordx4 v[34:35], off
	v_lshl_add_u64 v[34:35], v[90:91], 0, s[12:13]
	v_lshl_add_u64 v[34:35], v[34:35], 0, s[0:1]
	s_add_i32 m0, s87, 0x2000
	s_nop 0
	global_load_lds_dwordx4 v[34:35], off
.LBB0_1456:
	ds_read_b128 v[34:37], v140
	ds_read_b128 v[38:41], v140 offset:8192
	ds_read_b128 v[82:85], v141
	ds_read_b128 v[86:89], v141 offset:8192
	v_exp_f32_e32 v50, v50
	v_exp_f32_e32 v51, v51
	s_waitcnt lgkmcnt(0)
	v_mfma_f32_32x32x16_bf16 v[66:81], v[34:37], v[98:101], 0
	v_exp_f32_e32 v52, v52
	v_exp_f32_e32 v53, v53
	v_exp_f32_e32 v54, v54
	v_exp_f32_e32 v55, v55
	v_exp_f32_e32 v56, v56
	v_exp_f32_e32 v57, v57
	v_exp_f32_e32 v58, v58
	v_mfma_f32_32x32x16_bf16 v[34:49], v[38:41], v[98:101], 0
	v_exp_f32_e32 v59, v59
	v_exp_f32_e32 v60, v60
	v_exp_f32_e32 v61, v61
	v_exp_f32_e32 v62, v62
	v_exp_f32_e32 v63, v63
	v_exp_f32_e32 v64, v64
	v_exp_f32_e32 v65, v65
	v_mfma_f32_32x32x16_bf16 v[66:81], v[82:85], v[102:105], v[66:81]
	v_add_f32_e32 v0, 0, v158
	v_add_f32_e32 v0, v159, v0
	v_add_f32_e32 v0, v160, v0
	v_add_f32_e32 v0, v161, v0
	v_add_f32_e32 v0, v162, v0
	v_add_f32_e32 v0, v163, v0
	v_add_f32_e32 v0, v166, v0
	v_mfma_f32_32x32x16_bf16 v[34:49], v[86:89], v[102:105], v[34:49]
	s_cmp_eq_u32 s93, 0
	s_cbranch_scc1 .Lmstag_3
	s_add_i32 s32, s92, 4
	s_cmp_ge_u32 s32, s89
	s_cbranch_scc1 .Lmstag_3
	v_lshl_add_u64 v[240:241], v[92:93], 0, s[12:13]
	s_mov_b64 s[96:97], 0x2a81b000
	s_mov_b32 m0, s83
	v_lshl_add_u64 v[240:241], v[240:241], 0, s[96:97]
	global_load_lds_dwordx4 v[240:241], off
	v_lshl_add_u64 v[240:241], v[94:95], 0, s[12:13]
	v_lshl_add_u64 v[240:241], v[240:241], 0, s[96:97]
	s_mov_b32 m0, s84
	s_mov_b64 s[96:97], 0x30e12000
	global_load_lds_dwordx4 v[240:241], off
	v_lshl_add_u64 v[240:241], v[90:91], 0, s[12:13]
	v_lshl_add_u64 v[240:241], v[240:241], 0, s[96:97]
	s_add_i32 m0, s87, 0x2000
	s_nop 0
	global_load_lds_dwordx4 v[240:241], off
.Lmstag_3:
	ds_read_b128 v[82:85], v142
	ds_read_b128 v[86:89], v142 offset:8192
	v_add_f32_e32 v0, v167, v0
	v_add_f32_e32 v0, v168, v0
	v_add_f32_e32 v0, v169, v0
	v_add_f32_e32 v0, v170, v0
	v_add_f32_e32 v0, v171, v0
	v_add_f32_e32 v0, v172, v0
	s_waitcnt lgkmcnt(0)
	v_mfma_f32_32x32x16_bf16 v[66:81], v[82:85], v[106:109], v[66:81]
	v_add_f32_e32 v0, v173, v0
	v_add_f32_e32 v0, v174, v0
	v_add_f32_e32 v0, v175, v0
	v_add_f32_e32 v0, v50, v0
	v_add_f32_e32 v0, v51, v0
	v_add_f32_e32 v0, v52, v0
	v_add_f32_e32 v0, v53, v0
	v_mfma_f32_32x32x16_bf16 v[34:49], v[86:89], v[106:109], v[34:49]
	ds_read_b128 v[82:85], v143
	ds_read_b128 v[86:89], v143 offset:8192
	v_add_f32_e32 v0, v54, v0
	v_add_f32_e32 v0, v55, v0
	v_add_f32_e32 v0, v56, v0
	v_add_f32_e32 v0, v57, v0
	v_add_f32_e32 v0, v58, v0
	v_add_f32_e32 v0, v59, v0
	s_waitcnt lgkmcnt(0)
	v_mfma_f32_32x32x16_bf16 v[66:81], v[82:85], v[110:113], v[66:81]
	v_add_f32_e32 v0, v60, v0
	v_add_f32_e32 v0, v61, v0
	v_add_f32_e32 v0, v62, v0
	v_add_f32_e32 v0, v63, v0
	v_add_f32_e32 v0, v64, v0
	v_add_f32_e32 v0, v65, v0
	v_add_f32_e32 v145, v145, v0
	v_mfma_f32_32x32x16_bf16 v[34:49], v[86:89], v[110:113], v[34:49]
	ds_read_b128 v[82:85], v144
	ds_read_b128 v[86:89], v144 offset:8192
	s_waitcnt lgkmcnt(0)
	v_mfma_f32_32x32x16_bf16 v[66:81], v[82:85], v[114:117], v[66:81]
	v_mfma_f32_32x32x16_bf16 v[34:49], v[86:89], v[114:117], v[34:49]
	ds_read_b128 v[82:85], v148
	ds_read_b128 v[86:89], v148 offset:8192
	s_waitcnt lgkmcnt(0)
	v_mfma_f32_32x32x16_bf16 v[66:81], v[82:85], v[118:121], v[66:81]
	v_cvt_pk_bf16_f32 v82, v158, v159
	v_cvt_pk_bf16_f32 v83, v160, v161
	v_cvt_pk_bf16_f32 v84, v162, v163
	v_cvt_pk_bf16_f32 v85, v166, v167
	s_nop 0
	v_permlane32_swap_b32_e32 v82, v84
	v_mfma_f32_32x32x16_bf16 v[34:49], v[86:89], v[118:121], v[34:49]
	v_cvt_pk_bf16_f32 v86, v168, v169
	v_cvt_pk_bf16_f32 v87, v170, v171
	v_cvt_pk_bf16_f32 v88, v172, v173
	v_cvt_pk_bf16_f32 v89, v174, v175
	v_cvt_pk_bf16_f32 v122, v50, v51
	v_cvt_pk_bf16_f32 v123, v52, v53
	v_cvt_pk_bf16_f32 v124, v54, v55
	v_cvt_pk_bf16_f32 v125, v56, v57
	v_cvt_pk_bf16_f32 v150, v58, v59
	v_cvt_pk_bf16_f32 v151, v60, v61
	v_cvt_pk_bf16_f32 v152, v62, v63
	v_cvt_pk_bf16_f32 v153, v64, v65
	ds_read_b64_tr_b16 v[154:155], v97 offset:0
	ds_read_b64_tr_b16 v[156:157], v97 offset:0x400
	ds_read_b64_tr_b16 v[184:185], v97 offset:0x800
	ds_read_b64_tr_b16 v[186:187], v97 offset:0xc00
	ds_read_b64_tr_b16 v[188:189], v97 offset:0x1000
	ds_read_b64_tr_b16 v[190:191], v97 offset:0x1400
	ds_read_b64_tr_b16 v[192:193], v97 offset:0x1800
	ds_read_b64_tr_b16 v[194:195], v97 offset:0x1c00
	ds_read_b64_tr_b16 v[196:197], v97 offset:0x200
	ds_read_b64_tr_b16 v[198:199], v97 offset:0x600
	ds_read_b64_tr_b16 v[200:201], v97 offset:0xa00
	ds_read_b64_tr_b16 v[202:203], v97 offset:0xe00
	v_permlane32_swap_b32_e32 v83, v85
	ds_read_b64_tr_b16 v[204:205], v97 offset:0x1200
	ds_read_b64_tr_b16 v[206:207], v97 offset:0x1600
	ds_read_b64_tr_b16 v[208:209], v97 offset:0x1a00
	ds_read_b64_tr_b16 v[210:211], v97 offset:0x1e00
	s_waitcnt lgkmcnt(8)
	v_permlane32_swap_b32_e32 v86, v88
	s_nop 0
	v_mfma_f32_32x32x16_bf16 v[2:17], v[82:85], v[154:157], v[2:17]
	s_waitcnt lgkmcnt(0)
	v_permlane32_swap_b32_e32 v87, v89
	v_permlane32_swap_b32_e32 v122, v124
	v_permlane32_swap_b32_e32 v123, v125
	v_mfma_f32_32x32x16_bf16 v[18:33], v[82:85], v[196:199], v[18:33]
	v_permlane32_swap_b32_e32 v150, v152
	v_permlane32_swap_b32_e32 v151, v153
	v_exp_f32_e32 v196, v77
	v_exp_f32_e32 v198, v79
	v_exp_f32_e32 v197, v80
	v_mfma_f32_32x32x16_bf16 v[2:17], v[86:89], v[184:187], v[2:17]
	v_exp_f32_e32 v184, v66
	v_exp_f32_e32 v186, v67
	v_exp_f32_e32 v185, v68
	v_exp_f32_e32 v187, v69
	v_exp_f32_e32 v199, v81
	v_mfma_f32_32x32x16_bf16 v[18:33], v[86:89], v[200:203], v[18:33]
	v_mfma_f32_32x32x16_bf16 v[2:17], v[122:125], v[188:191], v[2:17]
	v_exp_f32_e32 v189, v70
	v_exp_f32_e32 v188, v74
	v_exp_f32_e32 v191, v75
	v_exp_f32_e32 v190, v76
	v_mfma_f32_32x32x16_bf16 v[18:33], v[122:125], v[204:207], v[18:33]
	v_mfma_f32_32x32x16_bf16 v[2:17], v[150:153], v[192:195], v[2:17]
	v_exp_f32_e32 v193, v71
	v_exp_f32_e32 v192, v72
	v_exp_f32_e32 v194, v73
	v_exp_f32_e32 v195, v78
	v_mfma_f32_32x32x16_bf16 v[18:33], v[150:153], v[208:211], v[18:33]
	s_cmp_ge_u32 s92, s90
	s_cbranch_scc1 .LBB0_1433

.LBB0_1459:
.LBB0_1461:
	s_add_i32 s0, s92, 5
	s_cmp_ge_u32 s0, s89
	s_waitcnt vmcnt(0)
	s_barrier
	s_cbranch_scc1 .LBB0_1432
	s_cmp_lg_u32 s93, 0
	s_cbranch_scc1 .LBB0_1432
	v_lshl_add_u64 v[50:51], v[92:93], 0, s[12:13]
	s_mov_b64 s[0:1], 0x2a81e000
	v_lshl_add_u64 v[50:51], v[50:51], 0, s[0:1]
	s_add_i32 m0, s81, 0x8000
	s_nop 0
	global_load_lds_dwordx4 v[50:51], off
	v_lshl_add_u64 v[50:51], v[94:95], 0, s[12:13]
	v_lshl_add_u64 v[50:51], v[50:51], 0, s[0:1]
	s_add_i32 m0, s81, 0x8400
	s_mov_b64 s[0:1], 0x30e14000
	global_load_lds_dwordx4 v[50:51], off
	v_lshl_add_u64 v[50:51], v[90:91], 0, s[12:13]
	v_lshl_add_u64 v[50:51], v[50:51], 0, s[0:1]
	s_add_i32 m0, s87, 0x4000
	s_nop 0
	global_load_lds_dwordx4 v[50:51], off
	s_branch .LBB0_1432
